# P6 epilogue pipelined (8 X loads in flight) + P5a/P5b epilogues touch all gate rows up front
# baseline (speedup 1.0000x reference)
; __device__ __forceinline__ unsigned cvt_pk_bf16(float lo, float hi) { unsigned r; asm volatile("v_cvt_pk_bf16_f32 %0, %1, %2" : "=v"(r) : "v"(lo), "v"(hi)); return r; }
; __device__ __forceinline__ float bf_lo(unsigned w) { return __uint_as_float(w << 16); }
; __device__ __forceinline__ float bf_hi(unsigned w) { return __uint_as_float(w & 0xffff0000u); }
;     __device__ __forceinline__ void operator()(const f32x4 (&acc)[2][2][4][2], const Unit& u, int wr, int wc, int fr, int fq) const {
;         const int row0 = u.pm * BM + wr * 64 + fr; const int col0 = u.pn * BM + wc * 32 + 8 * fq;
; #pragma unroll
;         for (int ai = 0; ai < 2; ++ai)
; #pragma unroll
;             for (int m = 0; m < 4; ++m) { const size_t row = (size_t)(row0 + ai * HALF + m * 16);
; #pragma unroll
;                 for (int bj = 0; bj < 2; ++bj) { const int col = col0 + bj * HALF; const u32x4 g = *(const u32x4*)(G + row * ldg + col);
;                     const f32x4 a0 = acc[ai][bj][m][0] * P5_ACC_SCALE, a1 = acc[ai][bj][m][1] * P5_ACC_SCALE;
;                     const f32x4 o0 = {a0[0] * bf_lo(g.x), a0[1] * bf_hi(g.x), a0[2] * bf_lo(g.y), a0[3] * bf_hi(g.y)};
;                     const f32x4 o1 = {a1[0] * bf_lo(g.z), a1[1] * bf_hi(g.z), a1[2] * bf_lo(g.w), a1[3] * bf_hi(g.w)};
;                     u32x4 w; w.x = cvt_pk_bf16(o0[0], o0[1]); w.y = cvt_pk_bf16(o0[2], o0[3]); w.z = cvt_pk_bf16(o1[0], o1[1]); w.w = cvt_pk_bf16(o1[2], o1[3]);
;                     *(u32x4*)(M1 + row * 2048 + col) = w; } }
.LBB0_733:
	v_lshl_or_b32 v2, s69, 8, v193
	v_lshl_add_u32 v4, s58, 8, v191
	v_mov_b64_e32 v[6:7], s[36:37]
	v_ashrrev_i32_e32 v3, 31, v2
	v_mad_i64_i32 v[8:9], s[60:61], v4, s68, v[6:7]
	v_lshlrev_b64 v[2:3], 1, v[2:3]
	v_lshl_add_u64 v[12:13], v[8:9], 0, v[2:3]
	v_mad_i64_i32 v[238:239], s[82:83], v4, s68, v[6:7]
	v_lshl_add_u64 v[238:239], v[238:239], 0, v[2:3]
	global_load_dword v240, v[238:239], off offset:256
	v_add_u32_e32 v236, 0x10, v4
	v_mad_i64_i32 v[238:239], s[82:83], v236, s68, v[6:7]
	v_lshl_add_u64 v[238:239], v[238:239], 0, v[2:3]
	global_load_dword v240, v[238:239], off
	global_load_dword v240, v[238:239], off offset:256
	v_add_u32_e32 v236, 0x20, v4
	v_mad_i64_i32 v[238:239], s[82:83], v236, s68, v[6:7]
	v_lshl_add_u64 v[238:239], v[238:239], 0, v[2:3]
	global_load_dword v240, v[238:239], off
	global_load_dword v240, v[238:239], off offset:256
	v_add_u32_e32 v236, 0x30, v4
	v_mad_i64_i32 v[238:239], s[82:83], v236, s68, v[6:7]
	v_lshl_add_u64 v[238:239], v[238:239], 0, v[2:3]
	global_load_dword v240, v[238:239], off
	global_load_dword v240, v[238:239], off offset:256
	v_add_u32_e32 v236, 0x80, v4
	v_mad_i64_i32 v[238:239], s[82:83], v236, s68, v[6:7]
	v_lshl_add_u64 v[238:239], v[238:239], 0, v[2:3]
	global_load_dword v240, v[238:239], off
	global_load_dword v240, v[238:239], off offset:256
	v_add_u32_e32 v236, 0x90, v4
	v_mad_i64_i32 v[238:239], s[82:83], v236, s68, v[6:7]
	v_lshl_add_u64 v[238:239], v[238:239], 0, v[2:3]
	global_load_dword v240, v[238:239], off
	global_load_dword v240, v[238:239], off offset:256
	v_add_u32_e32 v236, 0xa0, v4
	v_mad_i64_i32 v[238:239], s[82:83], v236, s68, v[6:7]
	v_lshl_add_u64 v[238:239], v[238:239], 0, v[2:3]
	global_load_dword v240, v[238:239], off
	global_load_dword v240, v[238:239], off offset:256
	v_add_u32_e32 v236, 0xb0, v4
	v_mad_i64_i32 v[238:239], s[82:83], v236, s68, v[6:7]
	v_lshl_add_u64 v[238:239], v[238:239], 0, v[2:3]
	global_load_dword v240, v[238:239], off
	global_load_dword v240, v[238:239], off offset:256
	global_load_dwordx4 v[8:11], v[12:13], off
	v_pk_mul_f32 v[14:15], v[160:161], s[42:43] op_sel_hi:[1,0]
	v_pk_mul_f32 v[16:17], v[158:159], s[42:43] op_sel_hi:[1,0]
	v_pk_mul_f32 v[18:19], v[156:157], s[42:43] op_sel_hi:[1,0]
	v_pk_mul_f32 v[20:21], v[154:155], s[42:43] op_sel_hi:[1,0]
	s_andn2_b64 vcc, exec, s[4:5]
	s_mov_b64 s[4:5], -1
	s_waitcnt vmcnt(0)
	v_lshlrev_b32_e32 v5, 16, v8
	v_and_b32_e32 v8, 0xffff0000, v8
	v_lshlrev_b32_e32 v22, 16, v9
	v_and_b32_e32 v9, 0xffff0000, v9
	v_lshlrev_b32_e32 v23, 16, v10
	v_and_b32_e32 v10, 0xffff0000, v10
	v_lshlrev_b32_e32 v24, 16, v11
	v_and_b32_e32 v11, 0xffff0000, v11
	v_mul_f32_e32 v8, v17, v8
	v_mul_f32_e32 v14, v14, v22
	v_mul_f32_e32 v9, v15, v9
	v_mul_f32_e32 v15, v20, v23
	v_mul_f32_e32 v10, v21, v10
	v_mul_f32_e32 v11, v19, v11
	v_mul_f32_e32 v5, v16, v5
	v_mul_f32_e32 v16, v18, v24
	v_cvt_pk_bf16_f32 v8, v5, v8
	v_cvt_pk_bf16_f32 v9, v14, v9
	v_cvt_pk_bf16_f32 v10, v15, v10
	v_cvt_pk_bf16_f32 v11, v16, v11
	global_load_dwordx4 v[12:15], v[12:13], off offset:256
	v_ashrrev_i32_e32 v5, 31, v4
	v_lshlrev_b64 v[26:27], 12, v[4:5]
	v_lshl_add_u64 v[26:27], s[8:9], 0, v[26:27]
	v_or_b32_e32 v24, 16, v4
	v_lshl_add_u64 v[26:27], v[26:27], 0, v[2:3]
	v_pk_mul_f32 v[16:17], v[152:153], s[42:43] op_sel_hi:[1,0]
	v_pk_mul_f32 v[18:19], v[150:151], s[42:43] op_sel_hi:[1,0]
	v_pk_mul_f32 v[20:21], v[148:149], s[42:43] op_sel_hi:[1,0]
	v_pk_mul_f32 v[22:23], v[146:147], s[42:43] op_sel_hi:[1,0]
	v_mad_i64_i32 v[28:29], s[60:61], v24, s68, v[6:7]
	global_store_dwordx4 v[26:27], v[8:11], off
	v_lshl_add_u64 v[28:29], v[28:29], 0, v[2:3]
	v_ashrrev_i32_e32 v25, 31, v24
	v_lshlrev_b64 v[24:25], 12, v[24:25]
	v_lshl_add_u64 v[24:25], s[8:9], 0, v[24:25]
	v_lshl_add_u64 v[24:25], v[24:25], 0, v[2:3]
	s_waitcnt vmcnt(1)
	v_lshlrev_b32_e32 v5, 16, v12
	v_and_b32_e32 v8, 0xffff0000, v12
	v_lshlrev_b32_e32 v9, 16, v13
	v_and_b32_e32 v10, 0xffff0000, v13
	v_lshlrev_b32_e32 v11, 16, v14
	v_and_b32_e32 v12, 0xffff0000, v14
	v_lshlrev_b32_e32 v13, 16, v15
	v_and_b32_e32 v14, 0xffff0000, v15
	v_mul_f32_e32 v8, v19, v8
	v_mul_f32_e32 v9, v16, v9
	v_mul_f32_e32 v10, v17, v10
	v_mul_f32_e32 v11, v22, v11
	v_mul_f32_e32 v12, v23, v12
	v_mul_f32_e32 v13, v20, v13
	v_mul_f32_e32 v14, v21, v14
	v_mul_f32_e32 v5, v18, v5
	v_cvt_pk_bf16_f32 v8, v5, v8
	v_cvt_pk_bf16_f32 v9, v9, v10
	v_cvt_pk_bf16_f32 v10, v11, v12
	v_cvt_pk_bf16_f32 v11, v13, v14
	global_load_dwordx4 v[12:15], v[28:29], off
	v_pk_mul_f32 v[16:17], v[144:145], s[42:43] op_sel_hi:[1,0]
	v_pk_mul_f32 v[18:19], v[142:143], s[42:43] op_sel_hi:[1,0]
	v_pk_mul_f32 v[20:21], v[140:141], s[42:43] op_sel_hi:[1,0]
	v_pk_mul_f32 v[22:23], v[138:139], s[42:43] op_sel_hi:[1,0]
	global_store_dwordx4 v[26:27], v[8:11], off offset:256
	v_or_b32_e32 v26, 32, v4
	v_ashrrev_i32_e32 v27, 31, v26
	s_waitcnt vmcnt(1)
	v_lshlrev_b32_e32 v5, 16, v12
	v_and_b32_e32 v8, 0xffff0000, v12
	v_lshlrev_b32_e32 v9, 16, v13
	v_and_b32_e32 v10, 0xffff0000, v13
	v_lshlrev_b32_e32 v11, 16, v14
	v_and_b32_e32 v12, 0xffff0000, v14
	v_lshlrev_b32_e32 v13, 16, v15
	v_and_b32_e32 v14, 0xffff0000, v15
	v_mul_f32_e32 v8, v19, v8
	v_mul_f32_e32 v9, v16, v9
	v_mul_f32_e32 v10, v17, v10
	v_mul_f32_e32 v11, v22, v11
	v_mul_f32_e32 v12, v23, v12
	v_mul_f32_e32 v13, v20, v13
	v_mul_f32_e32 v14, v21, v14
	v_mul_f32_e32 v5, v18, v5
	v_cvt_pk_bf16_f32 v8, v5, v8
	v_cvt_pk_bf16_f32 v9, v9, v10
	v_cvt_pk_bf16_f32 v10, v11, v12
	v_cvt_pk_bf16_f32 v11, v13, v14
	global_load_dwordx4 v[12:15], v[28:29], off offset:256
	v_pk_mul_f32 v[16:17], v[136:137], s[42:43] op_sel_hi:[1,0]
	v_pk_mul_f32 v[18:19], v[134:135], s[42:43] op_sel_hi:[1,0]
	v_pk_mul_f32 v[20:21], v[132:133], s[42:43] op_sel_hi:[1,0]
	v_pk_mul_f32 v[22:23], v[130:131], s[42:43] op_sel_hi:[1,0]
	v_mad_i64_i32 v[28:29], s[60:61], v26, s68, v[6:7]
	global_store_dwordx4 v[24:25], v[8:11], off
	v_lshl_add_u64 v[28:29], v[28:29], 0, v[2:3]
	v_lshlrev_b64 v[26:27], 12, v[26:27]
	v_lshl_add_u64 v[26:27], s[8:9], 0, v[26:27]
	v_lshl_add_u64 v[26:27], v[26:27], 0, v[2:3]
	s_waitcnt vmcnt(1)
; __device__ __forceinline__ unsigned cvt_pk_bf16(float lo, float hi) { unsigned r; asm volatile("v_cvt_pk_bf16_f32 %0, %1, %2" : "=v"(r) : "v"(lo), "v"(hi)); return r; }
; __device__ __forceinline__ float bf_lo(unsigned w) { return __uint_as_float(w << 16); }
; __device__ __forceinline__ float bf_hi(unsigned w) { return __uint_as_float(w & 0xffff0000u); }
;     __device__ __forceinline__ void operator()(const f32x4 (&acc)[2][2][4][2], const Unit& u, int wr, int wc, int fr, int fq) const {
;     ...
;         for (int ai = 0; ai < 2; ++ai)
; #pragma unroll
;             for (int m = 0; m < 4; ++m) { const size_t row = (size_t)(row0 + ai * HALF + m * 16);
; #pragma unroll
;                 for (int bj = 0; bj < 2; ++bj) { const int col = col0 + bj * HALF; const u32x4 g = *(const u32x4*)(G + row * ldg + col);
;                     const f32x4 a0 = acc[ai][bj][m][0] * P5_ACC_SCALE, a1 = acc[ai][bj][m][1] * P5_ACC_SCALE;
;                     const f32x4 o0 = {a0[0] * bf_lo(g.x), a0[1] * bf_hi(g.x), a0[2] * bf_lo(g.y), a0[3] * bf_hi(g.y)};
;                     const f32x4 o1 = {a1[0] * bf_lo(g.z), a1[1] * bf_hi(g.z), a1[2] * bf_lo(g.w), a1[3] * bf_hi(g.w)};
;                     u32x4 w; w.x = cvt_pk_bf16(o0[0], o0[1]); w.y = cvt_pk_bf16(o0[2], o0[3]); w.z = cvt_pk_bf16(o1[0], o1[1]); w.w = cvt_pk_bf16(o1[2], o1[3]);
;                     *(u32x4*)(M1 + row * 2048 + col) = w; } }
	v_lshlrev_b32_e32 v5, 16, v12
	v_and_b32_e32 v8, 0xffff0000, v12
	v_lshlrev_b32_e32 v9, 16, v13
	v_and_b32_e32 v10, 0xffff0000, v13
	v_lshlrev_b32_e32 v11, 16, v14
	v_and_b32_e32 v12, 0xffff0000, v14
	v_lshlrev_b32_e32 v13, 16, v15
	v_and_b32_e32 v14, 0xffff0000, v15
	v_mul_f32_e32 v8, v19, v8
	v_mul_f32_e32 v9, v16, v9
	v_mul_f32_e32 v10, v17, v10
	v_mul_f32_e32 v11, v22, v11
	v_mul_f32_e32 v12, v23, v12
	v_mul_f32_e32 v13, v20, v13
	v_mul_f32_e32 v14, v21, v14
	v_mul_f32_e32 v5, v18, v5
	v_cvt_pk_bf16_f32 v8, v5, v8
	v_cvt_pk_bf16_f32 v9, v9, v10
	v_cvt_pk_bf16_f32 v10, v11, v12
	v_cvt_pk_bf16_f32 v11, v13, v14
	global_load_dwordx4 v[12:15], v[28:29], off
	v_pk_mul_f32 v[16:17], v[128:129], s[42:43] op_sel_hi:[1,0]
	v_pk_mul_f32 v[18:19], v[126:127], s[42:43] op_sel_hi:[1,0]
	v_pk_mul_f32 v[20:21], v[124:125], s[42:43] op_sel_hi:[1,0]
	v_pk_mul_f32 v[22:23], v[122:123], s[42:43] op_sel_hi:[1,0]
	global_store_dwordx4 v[24:25], v[8:11], off offset:256
	v_or_b32_e32 v24, 48, v4
	v_ashrrev_i32_e32 v25, 31, v24
	s_waitcnt vmcnt(1)
	v_lshlrev_b32_e32 v5, 16, v12
	v_and_b32_e32 v8, 0xffff0000, v12
	v_lshlrev_b32_e32 v9, 16, v13
	v_and_b32_e32 v10, 0xffff0000, v13
	v_lshlrev_b32_e32 v11, 16, v14
	v_and_b32_e32 v12, 0xffff0000, v14
	v_lshlrev_b32_e32 v13, 16, v15
	v_and_b32_e32 v14, 0xffff0000, v15
	v_mul_f32_e32 v8, v19, v8
	v_mul_f32_e32 v9, v16, v9
	v_mul_f32_e32 v10, v17, v10
	v_mul_f32_e32 v11, v22, v11
	v_mul_f32_e32 v12, v23, v12
	v_mul_f32_e32 v13, v20, v13
	v_mul_f32_e32 v14, v21, v14
	v_mul_f32_e32 v5, v18, v5
	v_cvt_pk_bf16_f32 v8, v5, v8
	v_cvt_pk_bf16_f32 v9, v9, v10
	v_cvt_pk_bf16_f32 v10, v11, v12
	v_cvt_pk_bf16_f32 v11, v13, v14
	global_load_dwordx4 v[12:15], v[28:29], off offset:256
	v_pk_mul_f32 v[16:17], v[120:121], s[42:43] op_sel_hi:[1,0]
	v_pk_mul_f32 v[18:19], v[118:119], s[42:43] op_sel_hi:[1,0]
	v_pk_mul_f32 v[20:21], v[116:117], s[42:43] op_sel_hi:[1,0]
	v_pk_mul_f32 v[22:23], v[114:115], s[42:43] op_sel_hi:[1,0]
	v_mad_i64_i32 v[28:29], s[60:61], v24, s68, v[6:7]
	global_store_dwordx4 v[26:27], v[8:11], off
	v_lshl_add_u64 v[28:29], v[28:29], 0, v[2:3]
	v_lshlrev_b64 v[24:25], 12, v[24:25]
	v_lshl_add_u64 v[24:25], s[8:9], 0, v[24:25]
	v_lshl_add_u64 v[24:25], v[24:25], 0, v[2:3]
	s_waitcnt vmcnt(1)
	v_lshlrev_b32_e32 v5, 16, v12
	v_and_b32_e32 v8, 0xffff0000, v12
	v_lshlrev_b32_e32 v9, 16, v13
	v_and_b32_e32 v10, 0xffff0000, v13
	v_lshlrev_b32_e32 v11, 16, v14
	v_and_b32_e32 v12, 0xffff0000, v14
	v_lshlrev_b32_e32 v13, 16, v15
	v_and_b32_e32 v14, 0xffff0000, v15
	v_mul_f32_e32 v8, v19, v8
	v_mul_f32_e32 v9, v16, v9
	v_mul_f32_e32 v10, v17, v10
	v_mul_f32_e32 v11, v22, v11
	v_mul_f32_e32 v12, v23, v12
	v_mul_f32_e32 v13, v20, v13
	v_mul_f32_e32 v14, v21, v14
	v_mul_f32_e32 v5, v18, v5
	v_cvt_pk_bf16_f32 v8, v5, v8
	v_cvt_pk_bf16_f32 v9, v9, v10
	v_cvt_pk_bf16_f32 v10, v11, v12
	v_cvt_pk_bf16_f32 v11, v13, v14
	global_load_dwordx4 v[12:15], v[28:29], off
	v_pk_mul_f32 v[16:17], v[112:113], s[42:43] op_sel_hi:[1,0]
	v_pk_mul_f32 v[18:19], v[110:111], s[42:43] op_sel_hi:[1,0]
	v_pk_mul_f32 v[20:21], v[108:109], s[42:43] op_sel_hi:[1,0]
	v_pk_mul_f32 v[22:23], v[106:107], s[42:43] op_sel_hi:[1,0]
	global_store_dwordx4 v[26:27], v[8:11], off offset:256
	v_add_u32_e32 v26, 0x80, v4
	v_ashrrev_i32_e32 v27, 31, v26
	s_waitcnt vmcnt(1)
	v_lshlrev_b32_e32 v5, 16, v12
	v_and_b32_e32 v8, 0xffff0000, v12
	v_lshlrev_b32_e32 v9, 16, v13
	v_and_b32_e32 v10, 0xffff0000, v13
	v_lshlrev_b32_e32 v11, 16, v14
	v_and_b32_e32 v12, 0xffff0000, v14
	v_lshlrev_b32_e32 v13, 16, v15
	v_and_b32_e32 v14, 0xffff0000, v15
	v_mul_f32_e32 v8, v19, v8
	v_mul_f32_e32 v9, v16, v9
	v_mul_f32_e32 v10, v17, v10
	v_mul_f32_e32 v11, v22, v11
	v_mul_f32_e32 v12, v23, v12
	v_mul_f32_e32 v13, v20, v13
	v_mul_f32_e32 v14, v21, v14
	v_mul_f32_e32 v5, v18, v5
	v_cvt_pk_bf16_f32 v8, v5, v8
	v_cvt_pk_bf16_f32 v9, v9, v10
	v_cvt_pk_bf16_f32 v10, v11, v12
	v_cvt_pk_bf16_f32 v11, v13, v14
	global_load_dwordx4 v[12:15], v[28:29], off offset:256
	v_pk_mul_f32 v[16:17], v[104:105], s[42:43] op_sel_hi:[1,0]
	v_pk_mul_f32 v[18:19], v[102:103], s[42:43] op_sel_hi:[1,0]
	v_pk_mul_f32 v[20:21], v[100:101], s[42:43] op_sel_hi:[1,0]
	v_pk_mul_f32 v[22:23], v[98:99], s[42:43] op_sel_hi:[1,0]
	v_mad_i64_i32 v[28:29], s[60:61], v26, s68, v[6:7]
	global_store_dwordx4 v[24:25], v[8:11], off
	v_lshl_add_u64 v[28:29], v[28:29], 0, v[2:3]
	v_lshlrev_b64 v[26:27], 12, v[26:27]
	v_lshl_add_u64 v[26:27], s[8:9], 0, v[26:27]
	v_lshl_add_u64 v[26:27], v[26:27], 0, v[2:3]
	s_waitcnt vmcnt(1)
	v_lshlrev_b32_e32 v5, 16, v12
	v_and_b32_e32 v8, 0xffff0000, v12
	v_lshlrev_b32_e32 v9, 16, v13
	v_and_b32_e32 v10, 0xffff0000, v13
	v_lshlrev_b32_e32 v11, 16, v14
	v_and_b32_e32 v12, 0xffff0000, v14
	v_lshlrev_b32_e32 v13, 16, v15
	v_and_b32_e32 v14, 0xffff0000, v15
	v_mul_f32_e32 v8, v19, v8
	v_mul_f32_e32 v9, v16, v9
	v_mul_f32_e32 v10, v17, v10
	v_mul_f32_e32 v11, v22, v11
	v_mul_f32_e32 v12, v23, v12
	v_mul_f32_e32 v13, v20, v13
	v_mul_f32_e32 v14, v21, v14
	v_mul_f32_e32 v5, v18, v5
	v_cvt_pk_bf16_f32 v8, v5, v8
	v_cvt_pk_bf16_f32 v9, v9, v10
	v_cvt_pk_bf16_f32 v10, v11, v12
	v_cvt_pk_bf16_f32 v11, v13, v14
	global_load_dwordx4 v[12:15], v[28:29], off
	v_pk_mul_f32 v[16:17], v[96:97], s[42:43] op_sel_hi:[1,0]
	v_pk_mul_f32 v[18:19], v[94:95], s[42:43] op_sel_hi:[1,0]
	v_pk_mul_f32 v[20:21], v[92:93], s[42:43] op_sel_hi:[1,0]
	v_pk_mul_f32 v[22:23], v[90:91], s[42:43] op_sel_hi:[1,0]
	global_store_dwordx4 v[24:25], v[8:11], off offset:256
	v_add_u32_e32 v24, 0x90, v4
	v_ashrrev_i32_e32 v25, 31, v24
	s_waitcnt vmcnt(1)
; __device__ __forceinline__ unsigned cvt_pk_bf16(float lo, float hi) { unsigned r; asm volatile("v_cvt_pk_bf16_f32 %0, %1, %2" : "=v"(r) : "v"(lo), "v"(hi)); return r; }
; __device__ __forceinline__ float bf_lo(unsigned w) { return __uint_as_float(w << 16); }
; __device__ __forceinline__ float bf_hi(unsigned w) { return __uint_as_float(w & 0xffff0000u); }
;     __device__ __forceinline__ void operator()(const f32x4 (&acc)[2][2][4][2], const Unit& u, int wr, int wc, int fr, int fq) const {
;     ...
;         for (int ai = 0; ai < 2; ++ai)
; #pragma unroll
;             for (int m = 0; m < 4; ++m) { const size_t row = (size_t)(row0 + ai * HALF + m * 16);
; #pragma unroll
;                 for (int bj = 0; bj < 2; ++bj) { const int col = col0 + bj * HALF; const u32x4 g = *(const u32x4*)(G + row * ldg + col);
;                     const f32x4 a0 = acc[ai][bj][m][0] * P5_ACC_SCALE, a1 = acc[ai][bj][m][1] * P5_ACC_SCALE;
;                     const f32x4 o0 = {a0[0] * bf_lo(g.x), a0[1] * bf_hi(g.x), a0[2] * bf_lo(g.y), a0[3] * bf_hi(g.y)};
;                     const f32x4 o1 = {a1[0] * bf_lo(g.z), a1[1] * bf_hi(g.z), a1[2] * bf_lo(g.w), a1[3] * bf_hi(g.w)};
;                     u32x4 w; w.x = cvt_pk_bf16(o0[0], o0[1]); w.y = cvt_pk_bf16(o0[2], o0[3]); w.z = cvt_pk_bf16(o1[0], o1[1]); w.w = cvt_pk_bf16(o1[2], o1[3]);
;                     *(u32x4*)(M1 + row * 2048 + col) = w; } }
	v_lshlrev_b32_e32 v5, 16, v12
	v_and_b32_e32 v8, 0xffff0000, v12
	v_lshlrev_b32_e32 v9, 16, v13
	v_and_b32_e32 v10, 0xffff0000, v13
	v_lshlrev_b32_e32 v11, 16, v14
	v_and_b32_e32 v12, 0xffff0000, v14
	v_lshlrev_b32_e32 v13, 16, v15
	v_and_b32_e32 v14, 0xffff0000, v15
	v_mul_f32_e32 v8, v19, v8
	v_mul_f32_e32 v9, v16, v9
	v_mul_f32_e32 v10, v17, v10
	v_mul_f32_e32 v11, v22, v11
	v_mul_f32_e32 v12, v23, v12
	v_mul_f32_e32 v13, v20, v13
	v_mul_f32_e32 v14, v21, v14
	v_mul_f32_e32 v5, v18, v5
	v_cvt_pk_bf16_f32 v8, v5, v8
	v_cvt_pk_bf16_f32 v9, v9, v10
	v_cvt_pk_bf16_f32 v10, v11, v12
	v_cvt_pk_bf16_f32 v11, v13, v14
	global_load_dwordx4 v[12:15], v[28:29], off offset:256
	v_pk_mul_f32 v[16:17], v[88:89], s[42:43] op_sel_hi:[1,0]
	v_pk_mul_f32 v[18:19], v[86:87], s[42:43] op_sel_hi:[1,0]
	v_pk_mul_f32 v[20:21], v[84:85], s[42:43] op_sel_hi:[1,0]
	v_pk_mul_f32 v[22:23], v[82:83], s[42:43] op_sel_hi:[1,0]
	v_mad_i64_i32 v[28:29], s[60:61], v24, s68, v[6:7]
	global_store_dwordx4 v[26:27], v[8:11], off
	v_lshl_add_u64 v[28:29], v[28:29], 0, v[2:3]
	v_lshlrev_b64 v[24:25], 12, v[24:25]
	v_lshl_add_u64 v[24:25], s[8:9], 0, v[24:25]
	v_lshl_add_u64 v[24:25], v[24:25], 0, v[2:3]
	s_waitcnt vmcnt(1)
	v_lshlrev_b32_e32 v5, 16, v12
	v_and_b32_e32 v8, 0xffff0000, v12
	v_lshlrev_b32_e32 v9, 16, v13
	v_and_b32_e32 v10, 0xffff0000, v13
	v_lshlrev_b32_e32 v11, 16, v14
	v_and_b32_e32 v12, 0xffff0000, v14
	v_lshlrev_b32_e32 v13, 16, v15
	v_and_b32_e32 v14, 0xffff0000, v15
	v_mul_f32_e32 v8, v19, v8
	v_mul_f32_e32 v9, v16, v9
	v_mul_f32_e32 v10, v17, v10
	v_mul_f32_e32 v11, v22, v11
	v_mul_f32_e32 v12, v23, v12
	v_mul_f32_e32 v13, v20, v13
	v_mul_f32_e32 v14, v21, v14
	v_mul_f32_e32 v5, v18, v5
	v_cvt_pk_bf16_f32 v8, v5, v8
	v_cvt_pk_bf16_f32 v9, v9, v10
	v_cvt_pk_bf16_f32 v10, v11, v12
	v_cvt_pk_bf16_f32 v11, v13, v14
	global_load_dwordx4 v[12:15], v[28:29], off
	v_pk_mul_f32 v[16:17], v[80:81], s[42:43] op_sel_hi:[1,0]
	v_pk_mul_f32 v[18:19], v[78:79], s[42:43] op_sel_hi:[1,0]
	v_pk_mul_f32 v[20:21], v[76:77], s[42:43] op_sel_hi:[1,0]
	v_pk_mul_f32 v[22:23], v[74:75], s[42:43] op_sel_hi:[1,0]
	global_store_dwordx4 v[26:27], v[8:11], off offset:256
	v_add_u32_e32 v26, 0xa0, v4
	v_ashrrev_i32_e32 v27, 31, v26
	s_waitcnt vmcnt(1)
	v_lshlrev_b32_e32 v5, 16, v12
	v_and_b32_e32 v8, 0xffff0000, v12
	v_lshlrev_b32_e32 v9, 16, v13
	v_and_b32_e32 v10, 0xffff0000, v13
	v_lshlrev_b32_e32 v11, 16, v14
	v_and_b32_e32 v12, 0xffff0000, v14
	v_lshlrev_b32_e32 v13, 16, v15
	v_and_b32_e32 v14, 0xffff0000, v15
	v_mul_f32_e32 v8, v19, v8
	v_mul_f32_e32 v9, v16, v9
	v_mul_f32_e32 v10, v17, v10
	v_mul_f32_e32 v11, v22, v11
	v_mul_f32_e32 v12, v23, v12
	v_mul_f32_e32 v13, v20, v13
	v_mul_f32_e32 v14, v21, v14
	v_mul_f32_e32 v5, v18, v5
	v_cvt_pk_bf16_f32 v8, v5, v8
	v_cvt_pk_bf16_f32 v9, v9, v10
	v_cvt_pk_bf16_f32 v10, v11, v12
	v_cvt_pk_bf16_f32 v11, v13, v14
	global_load_dwordx4 v[12:15], v[28:29], off offset:256
	v_pk_mul_f32 v[16:17], v[72:73], s[42:43] op_sel_hi:[1,0]
	v_pk_mul_f32 v[18:19], v[70:71], s[42:43] op_sel_hi:[1,0]
	v_pk_mul_f32 v[20:21], v[68:69], s[42:43] op_sel_hi:[1,0]
	v_pk_mul_f32 v[22:23], v[66:67], s[42:43] op_sel_hi:[1,0]
	v_mad_i64_i32 v[28:29], s[60:61], v26, s68, v[6:7]
	global_store_dwordx4 v[24:25], v[8:11], off
	v_lshl_add_u64 v[28:29], v[28:29], 0, v[2:3]
	s_waitcnt vmcnt(1)
	v_lshlrev_b32_e32 v5, 16, v12
	v_and_b32_e32 v8, 0xffff0000, v12
	v_lshlrev_b32_e32 v9, 16, v13
	v_and_b32_e32 v10, 0xffff0000, v13
	v_lshlrev_b32_e32 v11, 16, v14
	v_and_b32_e32 v12, 0xffff0000, v14
	v_lshlrev_b32_e32 v13, 16, v15
	v_and_b32_e32 v14, 0xffff0000, v15
	v_mul_f32_e32 v8, v19, v8
	v_mul_f32_e32 v9, v16, v9
	v_mul_f32_e32 v10, v17, v10
	v_mul_f32_e32 v11, v22, v11
	v_mul_f32_e32 v12, v23, v12
	v_mul_f32_e32 v13, v20, v13
	v_mul_f32_e32 v14, v21, v14
	v_mul_f32_e32 v5, v18, v5
	v_cvt_pk_bf16_f32 v8, v5, v8
	v_cvt_pk_bf16_f32 v9, v9, v10
	v_cvt_pk_bf16_f32 v10, v11, v12
	v_cvt_pk_bf16_f32 v11, v13, v14
	global_load_dwordx4 v[12:15], v[28:29], off
	v_pk_mul_f32 v[16:17], v[64:65], s[42:43] op_sel_hi:[1,0]
	v_pk_mul_f32 v[18:19], v[62:63], s[42:43] op_sel_hi:[1,0]
	v_pk_mul_f32 v[20:21], v[60:61], s[42:43] op_sel_hi:[1,0]
	v_pk_mul_f32 v[22:23], v[58:59], s[42:43] op_sel_hi:[1,0]
	global_store_dwordx4 v[24:25], v[8:11], off offset:256
	v_add_u32_e32 v24, 0xb0, v4
	v_ashrrev_i32_e32 v25, 31, v24
	s_waitcnt vmcnt(1)
; __device__ __forceinline__ unsigned cvt_pk_bf16(float lo, float hi) { unsigned r; asm volatile("v_cvt_pk_bf16_f32 %0, %1, %2" : "=v"(r) : "v"(lo), "v"(hi)); return r; }
; __device__ __forceinline__ float bf_lo(unsigned w) { return __uint_as_float(w << 16); }
; __device__ __forceinline__ float bf_hi(unsigned w) { return __uint_as_float(w & 0xffff0000u); }
;     __device__ __forceinline__ void operator()(const f32x4 (&acc)[2][2][4][2], const Unit& u, int wr, int wc, int fr, int fq) const {
;     ...
;         for (int ai = 0; ai < 2; ++ai)
; #pragma unroll
;             for (int m = 0; m < 4; ++m) { const size_t row = (size_t)(row0 + ai * HALF + m * 16);
; #pragma unroll
;                 for (int bj = 0; bj < 2; ++bj) { const int col = col0 + bj * HALF; const u32x4 g = *(const u32x4*)(G + row * ldg + col);
;                     const f32x4 a0 = acc[ai][bj][m][0] * P5_ACC_SCALE, a1 = acc[ai][bj][m][1] * P5_ACC_SCALE;
;                     const f32x4 o0 = {a0[0] * bf_lo(g.x), a0[1] * bf_hi(g.x), a0[2] * bf_lo(g.y), a0[3] * bf_hi(g.y)};
;                     const f32x4 o1 = {a1[0] * bf_lo(g.z), a1[1] * bf_hi(g.z), a1[2] * bf_lo(g.w), a1[3] * bf_hi(g.w)};
;                     u32x4 w; w.x = cvt_pk_bf16(o0[0], o0[1]); w.y = cvt_pk_bf16(o0[2], o0[3]); w.z = cvt_pk_bf16(o1[0], o1[1]); w.w = cvt_pk_bf16(o1[2], o1[3]);
;                     *(u32x4*)(M1 + row * 2048 + col) = w; } }
	v_lshlrev_b32_e32 v5, 16, v12
	v_and_b32_e32 v8, 0xffff0000, v12
	v_lshlrev_b32_e32 v9, 16, v13
	v_and_b32_e32 v10, 0xffff0000, v13
	v_lshlrev_b32_e32 v11, 16, v14
	v_and_b32_e32 v12, 0xffff0000, v14
	v_lshlrev_b32_e32 v13, 16, v15
	v_and_b32_e32 v14, 0xffff0000, v15
	v_mul_f32_e32 v8, v19, v8
	v_mul_f32_e32 v9, v16, v9
	v_mul_f32_e32 v10, v17, v10
	v_mul_f32_e32 v11, v22, v11
	v_mul_f32_e32 v12, v23, v12
	v_mul_f32_e32 v13, v20, v13
	v_mul_f32_e32 v14, v21, v14
	v_mul_f32_e32 v5, v18, v5
	v_cvt_pk_bf16_f32 v8, v5, v8
	v_cvt_pk_bf16_f32 v9, v9, v10
	v_cvt_pk_bf16_f32 v10, v11, v12
	v_cvt_pk_bf16_f32 v11, v13, v14
	global_load_dwordx4 v[12:15], v[28:29], off offset:256
	v_mad_i64_i32 v[4:5], s[60:61], v24, s68, v[6:7]
	v_lshlrev_b64 v[6:7], 12, v[26:27]
	v_lshl_add_u64 v[26:27], v[4:5], 0, v[2:3]
	v_lshl_add_u64 v[4:5], s[8:9], 0, v[6:7]
	v_lshl_add_u64 v[28:29], v[4:5], 0, v[2:3]
	v_pk_mul_f32 v[16:17], v[56:57], s[42:43] op_sel_hi:[1,0]
	v_pk_mul_f32 v[18:19], v[54:55], s[42:43] op_sel_hi:[1,0]
	v_pk_mul_f32 v[20:21], v[52:53], s[42:43] op_sel_hi:[1,0]
	v_pk_mul_f32 v[22:23], v[50:51], s[42:43] op_sel_hi:[1,0]
	global_store_dwordx4 v[28:29], v[8:11], off
	s_waitcnt vmcnt(1)
	v_lshlrev_b32_e32 v4, 16, v12
	v_and_b32_e32 v5, 0xffff0000, v12
	v_lshlrev_b32_e32 v6, 16, v13
	v_and_b32_e32 v7, 0xffff0000, v13
	v_lshlrev_b32_e32 v8, 16, v14
	v_and_b32_e32 v9, 0xffff0000, v14
	v_lshlrev_b32_e32 v10, 16, v15
	v_and_b32_e32 v11, 0xffff0000, v15
	v_mul_f32_e32 v4, v18, v4
	v_mul_f32_e32 v5, v19, v5
	v_mul_f32_e32 v6, v16, v6
	v_mul_f32_e32 v7, v17, v7
	v_mul_f32_e32 v8, v22, v8
	v_mul_f32_e32 v9, v23, v9
	v_mul_f32_e32 v10, v20, v10
	v_mul_f32_e32 v11, v21, v11
	v_cvt_pk_bf16_f32 v4, v4, v5
	v_cvt_pk_bf16_f32 v5, v6, v7
	v_cvt_pk_bf16_f32 v6, v8, v9
	v_cvt_pk_bf16_f32 v7, v10, v11
	global_load_dwordx4 v[8:11], v[26:27], off
	v_pk_mul_f32 v[12:13], v[48:49], s[42:43] op_sel_hi:[1,0]
	v_pk_mul_f32 v[14:15], v[46:47], s[42:43] op_sel_hi:[1,0]
	v_pk_mul_f32 v[16:17], v[44:45], s[42:43] op_sel_hi:[1,0]
	v_pk_mul_f32 v[18:19], v[42:43], s[42:43] op_sel_hi:[1,0]
	global_store_dwordx4 v[28:29], v[4:7], off offset:256
	v_lshlrev_b64 v[20:21], 12, v[24:25]
	v_lshl_add_u64 v[20:21], s[8:9], 0, v[20:21]
	v_lshl_add_u64 v[20:21], v[20:21], 0, v[2:3]
	s_waitcnt vmcnt(1)
	v_lshlrev_b32_e32 v4, 16, v8
	v_and_b32_e32 v5, 0xffff0000, v8
	v_lshlrev_b32_e32 v6, 16, v9
	v_and_b32_e32 v7, 0xffff0000, v9
	v_lshlrev_b32_e32 v8, 16, v10
	v_and_b32_e32 v9, 0xffff0000, v10
	v_lshlrev_b32_e32 v10, 16, v11
	v_and_b32_e32 v11, 0xffff0000, v11
	v_mul_f32_e32 v4, v14, v4
	v_mul_f32_e32 v5, v15, v5
	v_mul_f32_e32 v6, v12, v6
	v_mul_f32_e32 v7, v13, v7
	v_mul_f32_e32 v8, v18, v8
	v_mul_f32_e32 v9, v19, v9
	v_mul_f32_e32 v10, v16, v10
	v_mul_f32_e32 v11, v17, v11
	v_cvt_pk_bf16_f32 v4, v4, v5
	v_cvt_pk_bf16_f32 v5, v6, v7
	v_cvt_pk_bf16_f32 v6, v8, v9
	v_cvt_pk_bf16_f32 v7, v10, v11
	global_load_dwordx4 v[8:11], v[26:27], off offset:256
	v_pk_mul_f32 v[12:13], v[40:41], s[42:43] op_sel_hi:[1,0]
	v_pk_mul_f32 v[14:15], v[38:39], s[42:43] op_sel_hi:[1,0]
	global_store_dwordx4 v[20:21], v[4:7], off
	v_pk_mul_f32 v[16:17], v[36:37], s[42:43] op_sel_hi:[1,0]
	v_pk_mul_f32 v[18:19], v[34:35], s[42:43] op_sel_hi:[1,0]
	s_waitcnt vmcnt(1)
	v_lshlrev_b32_e32 v2, 16, v8
	v_and_b32_e32 v3, 0xffff0000, v8
	v_lshlrev_b32_e32 v4, 16, v9
	v_and_b32_e32 v5, 0xffff0000, v9
	v_lshlrev_b32_e32 v6, 16, v10
	v_and_b32_e32 v7, 0xffff0000, v10
	v_lshlrev_b32_e32 v8, 16, v11
	v_and_b32_e32 v9, 0xffff0000, v11
	v_mul_f32_e32 v2, v14, v2
	v_mul_f32_e32 v3, v15, v3
	v_mul_f32_e32 v4, v12, v4
	v_mul_f32_e32 v5, v13, v5
	v_mul_f32_e32 v6, v18, v6
	v_mul_f32_e32 v7, v19, v7
	v_mul_f32_e32 v8, v16, v8
	v_mul_f32_e32 v9, v17, v9
	v_cvt_pk_bf16_f32 v2, v2, v3
	v_cvt_pk_bf16_f32 v3, v4, v5
	v_cvt_pk_bf16_f32 v4, v6, v7
	v_cvt_pk_bf16_f32 v5, v8, v9
	global_store_dwordx4 v[20:21], v[2:5], off offset:256
	s_cbranch_vccnz .LBB0_722
	s_andn2_b64 vcc, exec, s[22:23]
	s_cbranch_vccnz .LBB0_721
	s_barrier
	s_branch .LBB0_721

; __device__ __forceinline__ float bf_lo(unsigned w) { return __uint_as_float(w << 16); }
; __device__ __forceinline__ float bf_hi(unsigned w) { return __uint_as_float(w & 0xffff0000u); }
;     __device__ __forceinline__ void operator()(const f32x4 (&acc)[2][2][4][2], const Unit& u, int wr, int wc, int fr, int fq) const {
;     ...
;         for (int ai = 0; ai < 2; ++ai)
; #pragma unroll
;             for (int m = 0; m < 4; ++m) { const size_t row = (size_t)(row0 + ai * HALF + m * 16);
; #pragma unroll
;                 for (int bj = 0; bj < 2; ++bj) { const int col = col0 + bj * HALF; const u32x4 g = *(const u32x4*)(G + row * ldg + col);
;                     const u32x4 mw = *(const u32x4*)(M1 + row * 2048 + col);
;                     const f32x4 m0 = {bf_lo(mw.x), bf_hi(mw.x), bf_lo(mw.y), bf_hi(mw.y)}, m1 = {bf_lo(mw.z), bf_hi(mw.z), bf_lo(mw.w), bf_hi(mw.w)};
;                     const f32x4 a0 = acc[ai][bj][m][0] * P5_ACC_SCALE, a1 = acc[ai][bj][m][1] * P5_ACC_SCALE;
;                     const f32x4 o0 = {m0[0] + a0[0] * bf_lo(g.x), m0[1] + a0[1] * bf_hi(g.x), m0[2] + a0[2] * bf_lo(g.y), m0[3] + a0[3] * bf_hi(g.y)};
;                     const f32x4 o1 = {m1[0] + a1[0] * bf_lo(g.z), m1[1] + a1[1] * bf_hi(g.z), m1[2] + a1[2] * bf_lo(g.w), m1[3] + a1[3] * bf_hi(g.w)};
;                     int w0 = __builtin_amdgcn_cvt_pk_fp8_f32(o0[0] * 16.f, o0[1] * 16.f, 0, false); w0 = __builtin_amdgcn_cvt_pk_fp8_f32(o0[2] * 16.f, o0[3] * 16.f, w0, true);
;                     int w1 = __builtin_amdgcn_cvt_pk_fp8_f32(o1[0] * 16.f, o1[1] * 16.f, 0, false); w1 = __builtin_amdgcn_cvt_pk_fp8_f32(o1[2] * 16.f, o1[3] * 16.f, w1, true);
;                     typedef int v2i_m __attribute__((ext_vector_type(2))); *(v2i_m*)(MG + row * 2048 + col) = (v2i_m){w0, w1}; } }
.LBB0_753:
	v_lshl_add_u32 v8, s56, 8, v191
	v_lshl_or_b32 v2, s64, 8, v193
	v_ashrrev_i32_e32 v9, 31, v8
	v_mov_b64_e32 v[4:5], s[18:19]
	v_ashrrev_i32_e32 v3, 31, v2
	v_lshlrev_b64 v[14:15], 12, v[8:9]
	v_mad_i64_i32 v[10:11], s[58:59], v8, s57, v[4:5]
	v_lshlrev_b64 v[6:7], 1, v[2:3]
	v_lshl_add_u64 v[14:15], s[8:9], 0, v[14:15]
	v_lshl_add_u64 v[18:19], v[10:11], 0, v[6:7]
	v_lshl_add_u64 v[20:21], v[14:15], 0, v[6:7]
	v_mad_i64_i32 v[238:239], s[82:83], v8, s57, v[4:5]
	v_lshl_add_u64 v[238:239], v[238:239], 0, v[6:7]
	global_load_dword v240, v[238:239], off offset:256
	v_add_u32_e32 v236, 0x10, v8
	v_mad_i64_i32 v[238:239], s[82:83], v236, s57, v[4:5]
	v_lshl_add_u64 v[238:239], v[238:239], 0, v[6:7]
	global_load_dword v240, v[238:239], off
	global_load_dword v240, v[238:239], off offset:256
	v_add_u32_e32 v236, 0x20, v8
	v_mad_i64_i32 v[238:239], s[82:83], v236, s57, v[4:5]
	v_lshl_add_u64 v[238:239], v[238:239], 0, v[6:7]
	global_load_dword v240, v[238:239], off
	global_load_dword v240, v[238:239], off offset:256
	v_add_u32_e32 v236, 0x30, v8
	v_mad_i64_i32 v[238:239], s[82:83], v236, s57, v[4:5]
	v_lshl_add_u64 v[238:239], v[238:239], 0, v[6:7]
	global_load_dword v240, v[238:239], off
	global_load_dword v240, v[238:239], off offset:256
	v_add_u32_e32 v236, 0x80, v8
	v_mad_i64_i32 v[238:239], s[82:83], v236, s57, v[4:5]
	v_lshl_add_u64 v[238:239], v[238:239], 0, v[6:7]
	global_load_dword v240, v[238:239], off
	global_load_dword v240, v[238:239], off offset:256
	v_add_u32_e32 v236, 0x90, v8
	v_mad_i64_i32 v[238:239], s[82:83], v236, s57, v[4:5]
	v_lshl_add_u64 v[238:239], v[238:239], 0, v[6:7]
	global_load_dword v240, v[238:239], off
	global_load_dword v240, v[238:239], off offset:256
	v_add_u32_e32 v236, 0xa0, v8
	v_mad_i64_i32 v[238:239], s[82:83], v236, s57, v[4:5]
	v_lshl_add_u64 v[238:239], v[238:239], 0, v[6:7]
	global_load_dword v240, v[238:239], off
	global_load_dword v240, v[238:239], off offset:256
	v_add_u32_e32 v236, 0xb0, v8
	v_mad_i64_i32 v[238:239], s[82:83], v236, s57, v[4:5]
	v_lshl_add_u64 v[238:239], v[238:239], 0, v[6:7]
	global_load_dword v240, v[238:239], off
	global_load_dword v240, v[238:239], off offset:256
	global_load_dwordx4 v[10:13], v[18:19], off
	global_load_dwordx4 v[14:17], v[20:21], off
	v_pk_mul_f32 v[22:23], v[160:161], s[40:41] op_sel_hi:[1,0]
	v_pk_mul_f32 v[24:25], v[158:159], s[40:41] op_sel_hi:[1,0]
	v_pk_mul_f32 v[26:27], v[156:157], s[40:41] op_sel_hi:[1,0]
	v_pk_mul_f32 v[28:29], v[154:155], s[40:41] op_sel_hi:[1,0]
	v_mov_b32_e32 v30, 0
	v_mov_b32_e32 v31, 0
	s_andn2_b64 vcc, exec, s[4:5]
	s_mov_b64 s[4:5], -1
	s_waitcnt vmcnt(0)
	v_lshlrev_b32_e32 v32, 16, v10
	v_and_b32_e32 v10, 0xffff0000, v10
	v_lshlrev_b32_e32 v33, 16, v11
	v_and_b32_e32 v11, 0xffff0000, v11
	v_lshlrev_b32_e32 v154, 16, v12
	v_and_b32_e32 v12, 0xffff0000, v12
	v_lshlrev_b32_e32 v156, 16, v14
	v_and_b32_e32 v14, 0xffff0000, v14
	v_lshlrev_b32_e32 v157, 16, v15
	v_and_b32_e32 v15, 0xffff0000, v15
	v_lshlrev_b32_e32 v158, 16, v16
	v_and_b32_e32 v16, 0xffff0000, v16
	v_lshlrev_b32_e32 v155, 16, v13
	v_and_b32_e32 v13, 0xffff0000, v13
	v_lshlrev_b32_e32 v159, 16, v17
	v_and_b32_e32 v17, 0xffff0000, v17
	v_fmac_f32_e32 v156, v24, v32
	v_fmac_f32_e32 v14, v25, v10
	v_fmac_f32_e32 v15, v23, v11
	v_fmac_f32_e32 v158, v28, v154
	v_fmac_f32_e32 v16, v29, v12
	v_fmac_f32_e32 v17, v27, v13
	v_mul_f32_e32 v10, 0x41800000, v156
	v_mul_f32_e32 v11, 0x41800000, v14
	v_mul_f32_e32 v13, 0x41800000, v15
	v_mul_f32_e32 v14, 0x41800000, v158
	v_mul_f32_e32 v15, 0x41800000, v16
	v_cvt_pk_fp8_f32 v30, v10, v11
	v_cvt_pk_fp8_f32 v31, v14, v15
	v_fmac_f32_e32 v157, v22, v33
	v_fmac_f32_e32 v159, v26, v155
	v_mul_f32_e32 v12, 0x41800000, v157
	v_mul_f32_e32 v10, 0x41800000, v159
	v_mul_f32_e32 v11, 0x41800000, v17
	v_cvt_pk_fp8_f32 v30, v12, v13 op_sel:[0,0,1]
	v_cvt_pk_fp8_f32 v31, v10, v11 op_sel:[0,0,1]
	v_lshlrev_b64 v[10:11], 11, v[8:9]
	v_lshl_add_u64 v[10:11], s[22:23], 0, v[10:11]
	v_lshl_add_u64 v[22:23], v[10:11], 0, v[2:3]
	global_store_dwordx2 v[22:23], v[30:31], off
	global_load_dwordx4 v[10:13], v[20:21], off offset:256
	global_load_dwordx4 v[14:17], v[18:19], off offset:256
	v_pk_mul_f32 v[20:21], v[150:151], s[40:41] op_sel_hi:[1,0]
	v_pk_mul_f32 v[24:25], v[148:149], s[40:41] op_sel_hi:[1,0]
	v_pk_mul_f32 v[26:27], v[146:147], s[40:41] op_sel_hi:[1,0]
	v_pk_mul_f32 v[18:19], v[152:153], s[40:41] op_sel_hi:[1,0]
	v_mov_b32_e32 v28, 0
	v_mov_b32_e32 v29, 0
	v_or_b32_e32 v30, 16, v8
	v_ashrrev_i32_e32 v31, 31, v30
	s_waitcnt vmcnt(1)
	v_lshlrev_b32_e32 v9, 16, v10
	v_and_b32_e32 v10, 0xffff0000, v10
	v_lshlrev_b32_e32 v33, 16, v12
	v_and_b32_e32 v12, 0xffff0000, v12
	s_waitcnt vmcnt(0)
	v_lshlrev_b32_e32 v147, 16, v14
	v_and_b32_e32 v14, 0xffff0000, v14
	v_lshlrev_b32_e32 v149, 16, v16
	v_and_b32_e32 v16, 0xffff0000, v16
	v_lshlrev_b32_e32 v32, 16, v11
	v_and_b32_e32 v11, 0xffff0000, v11
	v_lshlrev_b32_e32 v148, 16, v15
	v_and_b32_e32 v15, 0xffff0000, v15
	v_fmac_f32_e32 v9, v20, v147
	v_fmac_f32_e32 v10, v21, v14
	v_fmac_f32_e32 v33, v26, v149
	v_fmac_f32_e32 v12, v27, v16
	v_fmac_f32_e32 v11, v19, v15
	v_mul_f32_e32 v9, 0x41800000, v9
	v_mul_f32_e32 v10, 0x41800000, v10
	v_mul_f32_e32 v15, 0x41800000, v33
	v_mul_f32_e32 v12, 0x41800000, v12
	v_cvt_pk_fp8_f32 v28, v9, v10
	v_cvt_pk_fp8_f32 v29, v15, v12
	v_lshlrev_b32_e32 v146, 16, v13
	v_and_b32_e32 v13, 0xffff0000, v13
	v_lshlrev_b32_e32 v150, 16, v17
	v_and_b32_e32 v17, 0xffff0000, v17
	v_fmac_f32_e32 v32, v18, v148
	v_fmac_f32_e32 v146, v24, v150
	v_fmac_f32_e32 v13, v25, v17
	v_mul_f32_e32 v14, 0x41800000, v32
	v_mul_f32_e32 v11, 0x41800000, v11
	v_mul_f32_e32 v9, 0x41800000, v146
	v_mul_f32_e32 v10, 0x41800000, v13
	v_cvt_pk_fp8_f32 v28, v14, v11 op_sel:[0,0,1]
	v_cvt_pk_fp8_f32 v29, v9, v10 op_sel:[0,0,1]
	v_lshlrev_b64 v[10:11], 12, v[30:31]
	v_lshl_add_u64 v[10:11], s[8:9], 0, v[10:11]
	v_mad_i64_i32 v[14:15], s[58:59], v30, s57, v[4:5]
	v_lshl_add_u64 v[18:19], v[10:11], 0, v[6:7]
	global_store_dwordx2 v[22:23], v[28:29], off offset:128
	v_lshl_add_u64 v[20:21], v[14:15], 0, v[6:7]
	global_load_dwordx4 v[10:13], v[18:19], off
	global_load_dwordx4 v[14:17], v[20:21], off
	v_pk_mul_f32 v[24:25], v[142:143], s[40:41] op_sel_hi:[1,0]
	v_pk_mul_f32 v[26:27], v[140:141], s[40:41] op_sel_hi:[1,0]
	v_pk_mul_f32 v[28:29], v[138:139], s[40:41] op_sel_hi:[1,0]
	v_pk_mul_f32 v[22:23], v[144:145], s[40:41] op_sel_hi:[1,0]
	v_mov_b32_e32 v32, 0
	v_mov_b32_e32 v33, 0
	s_waitcnt vmcnt(1)
; __device__ __forceinline__ float bf_lo(unsigned w) { return __uint_as_float(w << 16); }
; __device__ __forceinline__ float bf_hi(unsigned w) { return __uint_as_float(w & 0xffff0000u); }
;     __device__ __forceinline__ void operator()(const f32x4 (&acc)[2][2][4][2], const Unit& u, int wr, int wc, int fr, int fq) const {
;     ...
;             for (int m = 0; m < 4; ++m) { const size_t row = (size_t)(row0 + ai * HALF + m * 16);
; #pragma unroll
;                 for (int bj = 0; bj < 2; ++bj) { const int col = col0 + bj * HALF; const u32x4 g = *(const u32x4*)(G + row * ldg + col);
;                     const u32x4 mw = *(const u32x4*)(M1 + row * 2048 + col);
;                     const f32x4 m0 = {bf_lo(mw.x), bf_hi(mw.x), bf_lo(mw.y), bf_hi(mw.y)}, m1 = {bf_lo(mw.z), bf_hi(mw.z), bf_lo(mw.w), bf_hi(mw.w)};
;                     const f32x4 a0 = acc[ai][bj][m][0] * P5_ACC_SCALE, a1 = acc[ai][bj][m][1] * P5_ACC_SCALE;
;                     const f32x4 o0 = {m0[0] + a0[0] * bf_lo(g.x), m0[1] + a0[1] * bf_hi(g.x), m0[2] + a0[2] * bf_lo(g.y), m0[3] + a0[3] * bf_hi(g.y)};
;                     const f32x4 o1 = {m1[0] + a1[0] * bf_lo(g.z), m1[1] + a1[1] * bf_hi(g.z), m1[2] + a1[2] * bf_lo(g.w), m1[3] + a1[3] * bf_hi(g.w)};
;                     int w0 = __builtin_amdgcn_cvt_pk_fp8_f32(o0[0] * 16.f, o0[1] * 16.f, 0, false); w0 = __builtin_amdgcn_cvt_pk_fp8_f32(o0[2] * 16.f, o0[3] * 16.f, w0, true);
;                     int w1 = __builtin_amdgcn_cvt_pk_fp8_f32(o1[0] * 16.f, o1[1] * 16.f, 0, false); w1 = __builtin_amdgcn_cvt_pk_fp8_f32(o1[2] * 16.f, o1[3] * 16.f, w1, true);
;                     typedef int v2i_m __attribute__((ext_vector_type(2))); *(v2i_m*)(MG + row * 2048 + col) = (v2i_m){w0, w1}; } }
	v_lshlrev_b32_e32 v9, 16, v10
	v_and_b32_e32 v10, 0xffff0000, v10
	v_lshlrev_b32_e32 v139, 16, v12
	v_and_b32_e32 v12, 0xffff0000, v12
	s_waitcnt vmcnt(0)
	v_lshlrev_b32_e32 v141, 16, v14
	v_and_b32_e32 v14, 0xffff0000, v14
	v_lshlrev_b32_e32 v143, 16, v16
	v_and_b32_e32 v16, 0xffff0000, v16
	v_lshlrev_b32_e32 v138, 16, v11
	v_and_b32_e32 v11, 0xffff0000, v11
	v_lshlrev_b32_e32 v142, 16, v15
	v_and_b32_e32 v15, 0xffff0000, v15
	v_fmac_f32_e32 v9, v24, v141
	v_fmac_f32_e32 v10, v25, v14
	v_fmac_f32_e32 v139, v28, v143
	v_fmac_f32_e32 v12, v29, v16
	v_fmac_f32_e32 v11, v23, v15
	v_mul_f32_e32 v9, 0x41800000, v9
	v_mul_f32_e32 v10, 0x41800000, v10
	v_mul_f32_e32 v15, 0x41800000, v139
	v_mul_f32_e32 v12, 0x41800000, v12
	v_cvt_pk_fp8_f32 v32, v9, v10
	v_cvt_pk_fp8_f32 v33, v15, v12
	v_lshlrev_b32_e32 v140, 16, v13
	v_and_b32_e32 v13, 0xffff0000, v13
	v_lshlrev_b32_e32 v144, 16, v17
	v_and_b32_e32 v17, 0xffff0000, v17
	v_fmac_f32_e32 v138, v22, v142
	v_fmac_f32_e32 v140, v26, v144
	v_fmac_f32_e32 v13, v27, v17
	v_mul_f32_e32 v14, 0x41800000, v138
	v_mul_f32_e32 v11, 0x41800000, v11
	v_mul_f32_e32 v9, 0x41800000, v140
	v_mul_f32_e32 v10, 0x41800000, v13
	v_cvt_pk_fp8_f32 v32, v14, v11 op_sel:[0,0,1]
	v_cvt_pk_fp8_f32 v33, v9, v10 op_sel:[0,0,1]
	v_lshlrev_b64 v[10:11], 11, v[30:31]
	v_lshl_add_u64 v[10:11], s[22:23], 0, v[10:11]
	v_lshl_add_u64 v[22:23], v[10:11], 0, v[2:3]
	global_store_dwordx2 v[22:23], v[32:33], off
	global_load_dwordx4 v[10:13], v[18:19], off offset:256
	global_load_dwordx4 v[14:17], v[20:21], off offset:256
	v_pk_mul_f32 v[20:21], v[134:135], s[40:41] op_sel_hi:[1,0]
	v_pk_mul_f32 v[24:25], v[132:133], s[40:41] op_sel_hi:[1,0]
	v_pk_mul_f32 v[26:27], v[130:131], s[40:41] op_sel_hi:[1,0]
	v_pk_mul_f32 v[18:19], v[136:137], s[40:41] op_sel_hi:[1,0]
	v_mov_b32_e32 v28, 0
	v_mov_b32_e32 v29, 0
	v_or_b32_e32 v30, 32, v8
	v_ashrrev_i32_e32 v31, 31, v30
	s_waitcnt vmcnt(1)
	v_lshlrev_b32_e32 v9, 16, v10
	v_and_b32_e32 v10, 0xffff0000, v10
	v_lshlrev_b32_e32 v33, 16, v12
	v_and_b32_e32 v12, 0xffff0000, v12
	s_waitcnt vmcnt(0)
	v_lshlrev_b32_e32 v131, 16, v14
	v_and_b32_e32 v14, 0xffff0000, v14
	v_lshlrev_b32_e32 v133, 16, v16
	v_and_b32_e32 v16, 0xffff0000, v16
	v_lshlrev_b32_e32 v32, 16, v11
	v_and_b32_e32 v11, 0xffff0000, v11
	v_lshlrev_b32_e32 v132, 16, v15
	v_and_b32_e32 v15, 0xffff0000, v15
	v_fmac_f32_e32 v9, v20, v131
	v_fmac_f32_e32 v10, v21, v14
	v_fmac_f32_e32 v33, v26, v133
	v_fmac_f32_e32 v12, v27, v16
	v_fmac_f32_e32 v11, v19, v15
	v_mul_f32_e32 v9, 0x41800000, v9
	v_mul_f32_e32 v10, 0x41800000, v10
	v_mul_f32_e32 v15, 0x41800000, v33
	v_mul_f32_e32 v12, 0x41800000, v12
	v_cvt_pk_fp8_f32 v28, v9, v10
	v_cvt_pk_fp8_f32 v29, v15, v12
	v_lshlrev_b32_e32 v130, 16, v13
	v_and_b32_e32 v13, 0xffff0000, v13
	v_lshlrev_b32_e32 v134, 16, v17
	v_and_b32_e32 v17, 0xffff0000, v17
	v_fmac_f32_e32 v32, v18, v132
	v_fmac_f32_e32 v130, v24, v134
	v_fmac_f32_e32 v13, v25, v17
	v_mul_f32_e32 v14, 0x41800000, v32
	v_mul_f32_e32 v11, 0x41800000, v11
	v_mul_f32_e32 v9, 0x41800000, v130
	v_mul_f32_e32 v10, 0x41800000, v13
	v_cvt_pk_fp8_f32 v28, v14, v11 op_sel:[0,0,1]
	v_cvt_pk_fp8_f32 v29, v9, v10 op_sel:[0,0,1]
	v_lshlrev_b64 v[10:11], 12, v[30:31]
	v_lshl_add_u64 v[10:11], s[8:9], 0, v[10:11]
	v_mad_i64_i32 v[14:15], s[58:59], v30, s57, v[4:5]
	v_lshl_add_u64 v[18:19], v[10:11], 0, v[6:7]
	global_store_dwordx2 v[22:23], v[28:29], off offset:128
	v_lshl_add_u64 v[20:21], v[14:15], 0, v[6:7]
	global_load_dwordx4 v[10:13], v[18:19], off
	global_load_dwordx4 v[14:17], v[20:21], off
	v_pk_mul_f32 v[24:25], v[126:127], s[40:41] op_sel_hi:[1,0]
	v_pk_mul_f32 v[26:27], v[124:125], s[40:41] op_sel_hi:[1,0]
	v_pk_mul_f32 v[28:29], v[122:123], s[40:41] op_sel_hi:[1,0]
	v_pk_mul_f32 v[22:23], v[128:129], s[40:41] op_sel_hi:[1,0]
	v_mov_b32_e32 v32, 0
	v_mov_b32_e32 v33, 0
	s_waitcnt vmcnt(1)
	v_lshlrev_b32_e32 v9, 16, v10
	v_and_b32_e32 v10, 0xffff0000, v10
	v_lshlrev_b32_e32 v123, 16, v12
	v_and_b32_e32 v12, 0xffff0000, v12
	s_waitcnt vmcnt(0)
	v_lshlrev_b32_e32 v125, 16, v14
	v_and_b32_e32 v14, 0xffff0000, v14
	v_lshlrev_b32_e32 v127, 16, v16
	v_and_b32_e32 v16, 0xffff0000, v16
	v_lshlrev_b32_e32 v122, 16, v11
	v_and_b32_e32 v11, 0xffff0000, v11
	v_lshlrev_b32_e32 v126, 16, v15
	v_and_b32_e32 v15, 0xffff0000, v15
	v_fmac_f32_e32 v9, v24, v125
	v_fmac_f32_e32 v10, v25, v14
	v_fmac_f32_e32 v123, v28, v127
	v_fmac_f32_e32 v12, v29, v16
	v_fmac_f32_e32 v11, v23, v15
	v_mul_f32_e32 v9, 0x41800000, v9
	v_mul_f32_e32 v10, 0x41800000, v10
	v_mul_f32_e32 v15, 0x41800000, v123
	v_mul_f32_e32 v12, 0x41800000, v12
	v_cvt_pk_fp8_f32 v32, v9, v10
	v_cvt_pk_fp8_f32 v33, v15, v12
	v_lshlrev_b32_e32 v124, 16, v13
	v_and_b32_e32 v13, 0xffff0000, v13
	v_lshlrev_b32_e32 v128, 16, v17
	v_and_b32_e32 v17, 0xffff0000, v17
	v_fmac_f32_e32 v122, v22, v126
	v_fmac_f32_e32 v124, v26, v128
	v_fmac_f32_e32 v13, v27, v17
	v_mul_f32_e32 v14, 0x41800000, v122
	v_mul_f32_e32 v11, 0x41800000, v11
	v_mul_f32_e32 v9, 0x41800000, v124
	v_mul_f32_e32 v10, 0x41800000, v13
	v_cvt_pk_fp8_f32 v32, v14, v11 op_sel:[0,0,1]
	v_cvt_pk_fp8_f32 v33, v9, v10 op_sel:[0,0,1]
	v_lshlrev_b64 v[10:11], 11, v[30:31]
	v_lshl_add_u64 v[10:11], s[22:23], 0, v[10:11]
	v_lshl_add_u64 v[22:23], v[10:11], 0, v[2:3]
	global_store_dwordx2 v[22:23], v[32:33], off
	global_load_dwordx4 v[10:13], v[18:19], off offset:256
	global_load_dwordx4 v[14:17], v[20:21], off offset:256
	v_pk_mul_f32 v[20:21], v[118:119], s[40:41] op_sel_hi:[1,0]
	v_pk_mul_f32 v[24:25], v[116:117], s[40:41] op_sel_hi:[1,0]
	v_pk_mul_f32 v[26:27], v[114:115], s[40:41] op_sel_hi:[1,0]
	v_pk_mul_f32 v[18:19], v[120:121], s[40:41] op_sel_hi:[1,0]
	v_mov_b32_e32 v28, 0
	v_mov_b32_e32 v29, 0
	v_or_b32_e32 v30, 48, v8
	v_ashrrev_i32_e32 v31, 31, v30
	s_waitcnt vmcnt(1)
; __device__ __forceinline__ float bf_lo(unsigned w) { return __uint_as_float(w << 16); }
; __device__ __forceinline__ float bf_hi(unsigned w) { return __uint_as_float(w & 0xffff0000u); }
;     __device__ __forceinline__ void operator()(const f32x4 (&acc)[2][2][4][2], const Unit& u, int wr, int wc, int fr, int fq) const {
;     ...
;             for (int m = 0; m < 4; ++m) { const size_t row = (size_t)(row0 + ai * HALF + m * 16);
; #pragma unroll
;                 for (int bj = 0; bj < 2; ++bj) { const int col = col0 + bj * HALF; const u32x4 g = *(const u32x4*)(G + row * ldg + col);
;                     const u32x4 mw = *(const u32x4*)(M1 + row * 2048 + col);
;                     const f32x4 m0 = {bf_lo(mw.x), bf_hi(mw.x), bf_lo(mw.y), bf_hi(mw.y)}, m1 = {bf_lo(mw.z), bf_hi(mw.z), bf_lo(mw.w), bf_hi(mw.w)};
;                     const f32x4 a0 = acc[ai][bj][m][0] * P5_ACC_SCALE, a1 = acc[ai][bj][m][1] * P5_ACC_SCALE;
;                     const f32x4 o0 = {m0[0] + a0[0] * bf_lo(g.x), m0[1] + a0[1] * bf_hi(g.x), m0[2] + a0[2] * bf_lo(g.y), m0[3] + a0[3] * bf_hi(g.y)};
;                     const f32x4 o1 = {m1[0] + a1[0] * bf_lo(g.z), m1[1] + a1[1] * bf_hi(g.z), m1[2] + a1[2] * bf_lo(g.w), m1[3] + a1[3] * bf_hi(g.w)};
;                     int w0 = __builtin_amdgcn_cvt_pk_fp8_f32(o0[0] * 16.f, o0[1] * 16.f, 0, false); w0 = __builtin_amdgcn_cvt_pk_fp8_f32(o0[2] * 16.f, o0[3] * 16.f, w0, true);
;                     int w1 = __builtin_amdgcn_cvt_pk_fp8_f32(o1[0] * 16.f, o1[1] * 16.f, 0, false); w1 = __builtin_amdgcn_cvt_pk_fp8_f32(o1[2] * 16.f, o1[3] * 16.f, w1, true);
;                     typedef int v2i_m __attribute__((ext_vector_type(2))); *(v2i_m*)(MG + row * 2048 + col) = (v2i_m){w0, w1}; } }
	v_lshlrev_b32_e32 v9, 16, v10
	v_and_b32_e32 v10, 0xffff0000, v10
	v_lshlrev_b32_e32 v33, 16, v12
	v_and_b32_e32 v12, 0xffff0000, v12
	s_waitcnt vmcnt(0)
	v_lshlrev_b32_e32 v115, 16, v14
	v_and_b32_e32 v14, 0xffff0000, v14
	v_lshlrev_b32_e32 v117, 16, v16
	v_and_b32_e32 v16, 0xffff0000, v16
	v_lshlrev_b32_e32 v32, 16, v11
	v_and_b32_e32 v11, 0xffff0000, v11
	v_lshlrev_b32_e32 v116, 16, v15
	v_and_b32_e32 v15, 0xffff0000, v15
	v_fmac_f32_e32 v9, v20, v115
	v_fmac_f32_e32 v10, v21, v14
	v_fmac_f32_e32 v33, v26, v117
	v_fmac_f32_e32 v12, v27, v16
	v_fmac_f32_e32 v11, v19, v15
	v_mul_f32_e32 v9, 0x41800000, v9
	v_mul_f32_e32 v10, 0x41800000, v10
	v_mul_f32_e32 v15, 0x41800000, v33
	v_mul_f32_e32 v12, 0x41800000, v12
	v_cvt_pk_fp8_f32 v28, v9, v10
	v_cvt_pk_fp8_f32 v29, v15, v12
	v_lshlrev_b32_e32 v114, 16, v13
	v_and_b32_e32 v13, 0xffff0000, v13
	v_lshlrev_b32_e32 v118, 16, v17
	v_and_b32_e32 v17, 0xffff0000, v17
	v_fmac_f32_e32 v32, v18, v116
	v_fmac_f32_e32 v114, v24, v118
	v_fmac_f32_e32 v13, v25, v17
	v_mul_f32_e32 v14, 0x41800000, v32
	v_mul_f32_e32 v11, 0x41800000, v11
	v_mul_f32_e32 v9, 0x41800000, v114
	v_mul_f32_e32 v10, 0x41800000, v13
	v_cvt_pk_fp8_f32 v28, v14, v11 op_sel:[0,0,1]
	v_cvt_pk_fp8_f32 v29, v9, v10 op_sel:[0,0,1]
	v_lshlrev_b64 v[10:11], 12, v[30:31]
	v_lshl_add_u64 v[10:11], s[8:9], 0, v[10:11]
	v_mad_i64_i32 v[14:15], s[58:59], v30, s57, v[4:5]
	v_lshl_add_u64 v[18:19], v[10:11], 0, v[6:7]
	global_store_dwordx2 v[22:23], v[28:29], off offset:128
	v_lshl_add_u64 v[20:21], v[14:15], 0, v[6:7]
	global_load_dwordx4 v[10:13], v[18:19], off
	global_load_dwordx4 v[14:17], v[20:21], off
	v_pk_mul_f32 v[24:25], v[110:111], s[40:41] op_sel_hi:[1,0]
	v_pk_mul_f32 v[26:27], v[108:109], s[40:41] op_sel_hi:[1,0]
	v_pk_mul_f32 v[28:29], v[106:107], s[40:41] op_sel_hi:[1,0]
	v_pk_mul_f32 v[22:23], v[112:113], s[40:41] op_sel_hi:[1,0]
	v_mov_b32_e32 v32, 0
	v_mov_b32_e32 v33, 0
	s_waitcnt vmcnt(1)
	v_lshlrev_b32_e32 v9, 16, v10
	v_and_b32_e32 v10, 0xffff0000, v10
	v_lshlrev_b32_e32 v107, 16, v12
	v_and_b32_e32 v12, 0xffff0000, v12
	s_waitcnt vmcnt(0)
	v_lshlrev_b32_e32 v109, 16, v14
	v_and_b32_e32 v14, 0xffff0000, v14
	v_lshlrev_b32_e32 v111, 16, v16
	v_and_b32_e32 v16, 0xffff0000, v16
	v_lshlrev_b32_e32 v106, 16, v11
	v_and_b32_e32 v11, 0xffff0000, v11
	v_lshlrev_b32_e32 v110, 16, v15
	v_and_b32_e32 v15, 0xffff0000, v15
	v_fmac_f32_e32 v9, v24, v109
	v_fmac_f32_e32 v10, v25, v14
	v_fmac_f32_e32 v107, v28, v111
	v_fmac_f32_e32 v12, v29, v16
	v_fmac_f32_e32 v11, v23, v15
	v_mul_f32_e32 v9, 0x41800000, v9
	v_mul_f32_e32 v10, 0x41800000, v10
	v_mul_f32_e32 v15, 0x41800000, v107
	v_mul_f32_e32 v12, 0x41800000, v12
	v_cvt_pk_fp8_f32 v32, v9, v10
	v_cvt_pk_fp8_f32 v33, v15, v12
	v_lshlrev_b32_e32 v108, 16, v13
	v_and_b32_e32 v13, 0xffff0000, v13
	v_lshlrev_b32_e32 v112, 16, v17
	v_and_b32_e32 v17, 0xffff0000, v17
	v_fmac_f32_e32 v106, v22, v110
	v_fmac_f32_e32 v108, v26, v112
	v_fmac_f32_e32 v13, v27, v17
	v_mul_f32_e32 v14, 0x41800000, v106
	v_mul_f32_e32 v11, 0x41800000, v11
	v_mul_f32_e32 v9, 0x41800000, v108
	v_mul_f32_e32 v10, 0x41800000, v13
	v_cvt_pk_fp8_f32 v32, v14, v11 op_sel:[0,0,1]
	v_cvt_pk_fp8_f32 v33, v9, v10 op_sel:[0,0,1]
	v_lshlrev_b64 v[10:11], 11, v[30:31]
	v_lshl_add_u64 v[10:11], s[22:23], 0, v[10:11]
	v_lshl_add_u64 v[22:23], v[10:11], 0, v[2:3]
	global_store_dwordx2 v[22:23], v[32:33], off
	global_load_dwordx4 v[10:13], v[18:19], off offset:256
	global_load_dwordx4 v[14:17], v[20:21], off offset:256
	v_pk_mul_f32 v[20:21], v[102:103], s[40:41] op_sel_hi:[1,0]
	v_pk_mul_f32 v[24:25], v[100:101], s[40:41] op_sel_hi:[1,0]
	v_pk_mul_f32 v[26:27], v[98:99], s[40:41] op_sel_hi:[1,0]
	v_pk_mul_f32 v[18:19], v[104:105], s[40:41] op_sel_hi:[1,0]
	v_mov_b32_e32 v28, 0
	v_mov_b32_e32 v29, 0
	v_add_u32_e32 v30, 0x80, v8
	v_ashrrev_i32_e32 v31, 31, v30
	s_waitcnt vmcnt(1)
	v_lshlrev_b32_e32 v9, 16, v10
	v_and_b32_e32 v10, 0xffff0000, v10
	v_lshlrev_b32_e32 v33, 16, v12
	v_and_b32_e32 v12, 0xffff0000, v12
	s_waitcnt vmcnt(0)
	v_lshlrev_b32_e32 v99, 16, v14
	v_and_b32_e32 v14, 0xffff0000, v14
	v_lshlrev_b32_e32 v101, 16, v16
	v_and_b32_e32 v16, 0xffff0000, v16
	v_lshlrev_b32_e32 v32, 16, v11
	v_and_b32_e32 v11, 0xffff0000, v11
	v_lshlrev_b32_e32 v100, 16, v15
	v_and_b32_e32 v15, 0xffff0000, v15
	v_fmac_f32_e32 v9, v20, v99
	v_fmac_f32_e32 v10, v21, v14
	v_fmac_f32_e32 v33, v26, v101
	v_fmac_f32_e32 v12, v27, v16
	v_fmac_f32_e32 v11, v19, v15
	v_mul_f32_e32 v9, 0x41800000, v9
	v_mul_f32_e32 v10, 0x41800000, v10
	v_mul_f32_e32 v15, 0x41800000, v33
	v_mul_f32_e32 v12, 0x41800000, v12
	v_cvt_pk_fp8_f32 v28, v9, v10
	v_cvt_pk_fp8_f32 v29, v15, v12
	v_lshlrev_b32_e32 v98, 16, v13
	v_and_b32_e32 v13, 0xffff0000, v13
	v_lshlrev_b32_e32 v102, 16, v17
	v_and_b32_e32 v17, 0xffff0000, v17
	v_fmac_f32_e32 v32, v18, v100
	v_fmac_f32_e32 v98, v24, v102
	v_fmac_f32_e32 v13, v25, v17
	v_mul_f32_e32 v14, 0x41800000, v32
	v_mul_f32_e32 v11, 0x41800000, v11
	v_mul_f32_e32 v9, 0x41800000, v98
	v_mul_f32_e32 v10, 0x41800000, v13
	v_cvt_pk_fp8_f32 v28, v14, v11 op_sel:[0,0,1]
	v_cvt_pk_fp8_f32 v29, v9, v10 op_sel:[0,0,1]
	v_lshlrev_b64 v[10:11], 12, v[30:31]
	v_lshl_add_u64 v[10:11], s[8:9], 0, v[10:11]
	v_mad_i64_i32 v[14:15], s[58:59], v30, s57, v[4:5]
	v_lshl_add_u64 v[18:19], v[10:11], 0, v[6:7]
	global_store_dwordx2 v[22:23], v[28:29], off offset:128
	v_lshl_add_u64 v[20:21], v[14:15], 0, v[6:7]
	global_load_dwordx4 v[10:13], v[18:19], off
	global_load_dwordx4 v[14:17], v[20:21], off
	v_pk_mul_f32 v[24:25], v[94:95], s[40:41] op_sel_hi:[1,0]
	v_pk_mul_f32 v[26:27], v[92:93], s[40:41] op_sel_hi:[1,0]
	v_pk_mul_f32 v[28:29], v[90:91], s[40:41] op_sel_hi:[1,0]
	v_pk_mul_f32 v[22:23], v[96:97], s[40:41] op_sel_hi:[1,0]
	v_mov_b32_e32 v32, 0
	v_mov_b32_e32 v33, 0
	s_waitcnt vmcnt(1)
; __device__ __forceinline__ float bf_lo(unsigned w) { return __uint_as_float(w << 16); }
; __device__ __forceinline__ float bf_hi(unsigned w) { return __uint_as_float(w & 0xffff0000u); }
;     __device__ __forceinline__ void operator()(const f32x4 (&acc)[2][2][4][2], const Unit& u, int wr, int wc, int fr, int fq) const {
;     ...
;             for (int m = 0; m < 4; ++m) { const size_t row = (size_t)(row0 + ai * HALF + m * 16);
; #pragma unroll
;                 for (int bj = 0; bj < 2; ++bj) { const int col = col0 + bj * HALF; const u32x4 g = *(const u32x4*)(G + row * ldg + col);
;                     const u32x4 mw = *(const u32x4*)(M1 + row * 2048 + col);
;                     const f32x4 m0 = {bf_lo(mw.x), bf_hi(mw.x), bf_lo(mw.y), bf_hi(mw.y)}, m1 = {bf_lo(mw.z), bf_hi(mw.z), bf_lo(mw.w), bf_hi(mw.w)};
;                     const f32x4 a0 = acc[ai][bj][m][0] * P5_ACC_SCALE, a1 = acc[ai][bj][m][1] * P5_ACC_SCALE;
;                     const f32x4 o0 = {m0[0] + a0[0] * bf_lo(g.x), m0[1] + a0[1] * bf_hi(g.x), m0[2] + a0[2] * bf_lo(g.y), m0[3] + a0[3] * bf_hi(g.y)};
;                     const f32x4 o1 = {m1[0] + a1[0] * bf_lo(g.z), m1[1] + a1[1] * bf_hi(g.z), m1[2] + a1[2] * bf_lo(g.w), m1[3] + a1[3] * bf_hi(g.w)};
;                     int w0 = __builtin_amdgcn_cvt_pk_fp8_f32(o0[0] * 16.f, o0[1] * 16.f, 0, false); w0 = __builtin_amdgcn_cvt_pk_fp8_f32(o0[2] * 16.f, o0[3] * 16.f, w0, true);
;                     int w1 = __builtin_amdgcn_cvt_pk_fp8_f32(o1[0] * 16.f, o1[1] * 16.f, 0, false); w1 = __builtin_amdgcn_cvt_pk_fp8_f32(o1[2] * 16.f, o1[3] * 16.f, w1, true);
;                     typedef int v2i_m __attribute__((ext_vector_type(2))); *(v2i_m*)(MG + row * 2048 + col) = (v2i_m){w0, w1}; } }
	v_lshlrev_b32_e32 v9, 16, v10
	v_and_b32_e32 v10, 0xffff0000, v10
	v_lshlrev_b32_e32 v91, 16, v12
	v_and_b32_e32 v12, 0xffff0000, v12
	s_waitcnt vmcnt(0)
	v_lshlrev_b32_e32 v93, 16, v14
	v_and_b32_e32 v14, 0xffff0000, v14
	v_lshlrev_b32_e32 v95, 16, v16
	v_and_b32_e32 v16, 0xffff0000, v16
	v_lshlrev_b32_e32 v90, 16, v11
	v_and_b32_e32 v11, 0xffff0000, v11
	v_lshlrev_b32_e32 v94, 16, v15
	v_and_b32_e32 v15, 0xffff0000, v15
	v_fmac_f32_e32 v9, v24, v93
	v_fmac_f32_e32 v10, v25, v14
	v_fmac_f32_e32 v91, v28, v95
	v_fmac_f32_e32 v12, v29, v16
	v_fmac_f32_e32 v11, v23, v15
	v_mul_f32_e32 v9, 0x41800000, v9
	v_mul_f32_e32 v10, 0x41800000, v10
	v_mul_f32_e32 v15, 0x41800000, v91
	v_mul_f32_e32 v12, 0x41800000, v12
	v_cvt_pk_fp8_f32 v32, v9, v10
	v_cvt_pk_fp8_f32 v33, v15, v12
	v_lshlrev_b32_e32 v92, 16, v13
	v_and_b32_e32 v13, 0xffff0000, v13
	v_lshlrev_b32_e32 v96, 16, v17
	v_and_b32_e32 v17, 0xffff0000, v17
	v_fmac_f32_e32 v90, v22, v94
	v_fmac_f32_e32 v92, v26, v96
	v_fmac_f32_e32 v13, v27, v17
	v_mul_f32_e32 v14, 0x41800000, v90
	v_mul_f32_e32 v11, 0x41800000, v11
	v_mul_f32_e32 v9, 0x41800000, v92
	v_mul_f32_e32 v10, 0x41800000, v13
	v_cvt_pk_fp8_f32 v32, v14, v11 op_sel:[0,0,1]
	v_cvt_pk_fp8_f32 v33, v9, v10 op_sel:[0,0,1]
	v_lshlrev_b64 v[10:11], 11, v[30:31]
	v_lshl_add_u64 v[10:11], s[22:23], 0, v[10:11]
	v_lshl_add_u64 v[22:23], v[10:11], 0, v[2:3]
	global_store_dwordx2 v[22:23], v[32:33], off
	global_load_dwordx4 v[10:13], v[18:19], off offset:256
	global_load_dwordx4 v[14:17], v[20:21], off offset:256
	v_pk_mul_f32 v[20:21], v[86:87], s[40:41] op_sel_hi:[1,0]
	v_pk_mul_f32 v[24:25], v[84:85], s[40:41] op_sel_hi:[1,0]
	v_pk_mul_f32 v[26:27], v[82:83], s[40:41] op_sel_hi:[1,0]
	v_pk_mul_f32 v[18:19], v[88:89], s[40:41] op_sel_hi:[1,0]
	v_mov_b32_e32 v28, 0
	v_mov_b32_e32 v29, 0
	v_add_u32_e32 v30, 0x90, v8
	v_ashrrev_i32_e32 v31, 31, v30
	s_waitcnt vmcnt(1)
	v_lshlrev_b32_e32 v9, 16, v10
	v_and_b32_e32 v10, 0xffff0000, v10
	v_lshlrev_b32_e32 v33, 16, v12
	v_and_b32_e32 v12, 0xffff0000, v12
	s_waitcnt vmcnt(0)
	v_lshlrev_b32_e32 v83, 16, v14
	v_and_b32_e32 v14, 0xffff0000, v14
	v_lshlrev_b32_e32 v85, 16, v16
	v_and_b32_e32 v16, 0xffff0000, v16
	v_lshlrev_b32_e32 v32, 16, v11
	v_and_b32_e32 v11, 0xffff0000, v11
	v_lshlrev_b32_e32 v84, 16, v15
	v_and_b32_e32 v15, 0xffff0000, v15
	v_fmac_f32_e32 v9, v20, v83
	v_fmac_f32_e32 v10, v21, v14
	v_fmac_f32_e32 v33, v26, v85
	v_fmac_f32_e32 v12, v27, v16
	v_fmac_f32_e32 v11, v19, v15
	v_mul_f32_e32 v9, 0x41800000, v9
	v_mul_f32_e32 v10, 0x41800000, v10
	v_mul_f32_e32 v15, 0x41800000, v33
	v_mul_f32_e32 v12, 0x41800000, v12
	v_cvt_pk_fp8_f32 v28, v9, v10
	v_cvt_pk_fp8_f32 v29, v15, v12
	v_lshlrev_b32_e32 v82, 16, v13
	v_and_b32_e32 v13, 0xffff0000, v13
	v_lshlrev_b32_e32 v86, 16, v17
	v_and_b32_e32 v17, 0xffff0000, v17
	v_fmac_f32_e32 v32, v18, v84
	v_fmac_f32_e32 v82, v24, v86
	v_fmac_f32_e32 v13, v25, v17
	v_mul_f32_e32 v14, 0x41800000, v32
	v_mul_f32_e32 v11, 0x41800000, v11
	v_mul_f32_e32 v9, 0x41800000, v82
	v_mul_f32_e32 v10, 0x41800000, v13
	v_cvt_pk_fp8_f32 v28, v14, v11 op_sel:[0,0,1]
	v_cvt_pk_fp8_f32 v29, v9, v10 op_sel:[0,0,1]
	v_lshlrev_b64 v[10:11], 12, v[30:31]
	v_lshl_add_u64 v[10:11], s[8:9], 0, v[10:11]
	v_mad_i64_i32 v[14:15], s[58:59], v30, s57, v[4:5]
	v_lshl_add_u64 v[18:19], v[10:11], 0, v[6:7]
	global_store_dwordx2 v[22:23], v[28:29], off offset:128
	v_lshl_add_u64 v[20:21], v[14:15], 0, v[6:7]
	global_load_dwordx4 v[10:13], v[18:19], off
	global_load_dwordx4 v[14:17], v[20:21], off
	v_pk_mul_f32 v[24:25], v[78:79], s[40:41] op_sel_hi:[1,0]
	v_pk_mul_f32 v[26:27], v[76:77], s[40:41] op_sel_hi:[1,0]
	v_pk_mul_f32 v[28:29], v[74:75], s[40:41] op_sel_hi:[1,0]
	v_pk_mul_f32 v[22:23], v[80:81], s[40:41] op_sel_hi:[1,0]
	v_mov_b32_e32 v32, 0
	v_mov_b32_e32 v33, 0
	s_waitcnt vmcnt(1)
	v_lshlrev_b32_e32 v9, 16, v10
	v_and_b32_e32 v10, 0xffff0000, v10
	v_lshlrev_b32_e32 v75, 16, v12
	v_and_b32_e32 v12, 0xffff0000, v12
	s_waitcnt vmcnt(0)
	v_lshlrev_b32_e32 v77, 16, v14
	v_and_b32_e32 v14, 0xffff0000, v14
	v_lshlrev_b32_e32 v79, 16, v16
	v_and_b32_e32 v16, 0xffff0000, v16
	v_lshlrev_b32_e32 v74, 16, v11
	v_and_b32_e32 v11, 0xffff0000, v11
	v_lshlrev_b32_e32 v78, 16, v15
	v_and_b32_e32 v15, 0xffff0000, v15
	v_fmac_f32_e32 v9, v24, v77
	v_fmac_f32_e32 v10, v25, v14
	v_fmac_f32_e32 v75, v28, v79
	v_fmac_f32_e32 v12, v29, v16
	v_fmac_f32_e32 v11, v23, v15
	v_mul_f32_e32 v9, 0x41800000, v9
	v_mul_f32_e32 v10, 0x41800000, v10
	v_mul_f32_e32 v15, 0x41800000, v75
	v_mul_f32_e32 v12, 0x41800000, v12
	v_cvt_pk_fp8_f32 v32, v9, v10
	v_cvt_pk_fp8_f32 v33, v15, v12
	v_lshlrev_b32_e32 v76, 16, v13
	v_and_b32_e32 v13, 0xffff0000, v13
	v_lshlrev_b32_e32 v80, 16, v17
	v_and_b32_e32 v17, 0xffff0000, v17
	v_fmac_f32_e32 v74, v22, v78
	v_fmac_f32_e32 v76, v26, v80
	v_fmac_f32_e32 v13, v27, v17
	v_mul_f32_e32 v14, 0x41800000, v74
	v_mul_f32_e32 v11, 0x41800000, v11
	v_mul_f32_e32 v9, 0x41800000, v76
	v_mul_f32_e32 v10, 0x41800000, v13
	v_cvt_pk_fp8_f32 v32, v14, v11 op_sel:[0,0,1]
	v_cvt_pk_fp8_f32 v33, v9, v10 op_sel:[0,0,1]
	v_lshlrev_b64 v[10:11], 11, v[30:31]
	v_lshl_add_u64 v[10:11], s[22:23], 0, v[10:11]
	v_lshl_add_u64 v[22:23], v[10:11], 0, v[2:3]
	global_store_dwordx2 v[22:23], v[32:33], off
	global_load_dwordx4 v[10:13], v[18:19], off offset:256
	global_load_dwordx4 v[14:17], v[20:21], off offset:256
	v_pk_mul_f32 v[20:21], v[70:71], s[40:41] op_sel_hi:[1,0]
	v_pk_mul_f32 v[24:25], v[68:69], s[40:41] op_sel_hi:[1,0]
	v_pk_mul_f32 v[26:27], v[66:67], s[40:41] op_sel_hi:[1,0]
	v_pk_mul_f32 v[18:19], v[72:73], s[40:41] op_sel_hi:[1,0]
	v_mov_b32_e32 v28, 0
	v_mov_b32_e32 v29, 0
	v_add_u32_e32 v30, 0xa0, v8
	v_ashrrev_i32_e32 v31, 31, v30
	s_waitcnt vmcnt(1)
; __device__ __forceinline__ float bf_lo(unsigned w) { return __uint_as_float(w << 16); }
; __device__ __forceinline__ float bf_hi(unsigned w) { return __uint_as_float(w & 0xffff0000u); }
;     __device__ __forceinline__ void operator()(const f32x4 (&acc)[2][2][4][2], const Unit& u, int wr, int wc, int fr, int fq) const {
;     ...
;             for (int m = 0; m < 4; ++m) { const size_t row = (size_t)(row0 + ai * HALF + m * 16);
; #pragma unroll
;                 for (int bj = 0; bj < 2; ++bj) { const int col = col0 + bj * HALF; const u32x4 g = *(const u32x4*)(G + row * ldg + col);
;                     const u32x4 mw = *(const u32x4*)(M1 + row * 2048 + col);
;                     const f32x4 m0 = {bf_lo(mw.x), bf_hi(mw.x), bf_lo(mw.y), bf_hi(mw.y)}, m1 = {bf_lo(mw.z), bf_hi(mw.z), bf_lo(mw.w), bf_hi(mw.w)};
;                     const f32x4 a0 = acc[ai][bj][m][0] * P5_ACC_SCALE, a1 = acc[ai][bj][m][1] * P5_ACC_SCALE;
;                     const f32x4 o0 = {m0[0] + a0[0] * bf_lo(g.x), m0[1] + a0[1] * bf_hi(g.x), m0[2] + a0[2] * bf_lo(g.y), m0[3] + a0[3] * bf_hi(g.y)};
;                     const f32x4 o1 = {m1[0] + a1[0] * bf_lo(g.z), m1[1] + a1[1] * bf_hi(g.z), m1[2] + a1[2] * bf_lo(g.w), m1[3] + a1[3] * bf_hi(g.w)};
;                     int w0 = __builtin_amdgcn_cvt_pk_fp8_f32(o0[0] * 16.f, o0[1] * 16.f, 0, false); w0 = __builtin_amdgcn_cvt_pk_fp8_f32(o0[2] * 16.f, o0[3] * 16.f, w0, true);
;                     int w1 = __builtin_amdgcn_cvt_pk_fp8_f32(o1[0] * 16.f, o1[1] * 16.f, 0, false); w1 = __builtin_amdgcn_cvt_pk_fp8_f32(o1[2] * 16.f, o1[3] * 16.f, w1, true);
;                     typedef int v2i_m __attribute__((ext_vector_type(2))); *(v2i_m*)(MG + row * 2048 + col) = (v2i_m){w0, w1}; } }
	v_lshlrev_b32_e32 v9, 16, v10
	v_and_b32_e32 v10, 0xffff0000, v10
	v_lshlrev_b32_e32 v33, 16, v12
	v_and_b32_e32 v12, 0xffff0000, v12
	s_waitcnt vmcnt(0)
	v_lshlrev_b32_e32 v67, 16, v14
	v_and_b32_e32 v14, 0xffff0000, v14
	v_lshlrev_b32_e32 v69, 16, v16
	v_and_b32_e32 v16, 0xffff0000, v16
	v_lshlrev_b32_e32 v32, 16, v11
	v_and_b32_e32 v11, 0xffff0000, v11
	v_lshlrev_b32_e32 v68, 16, v15
	v_and_b32_e32 v15, 0xffff0000, v15
	v_fmac_f32_e32 v9, v20, v67
	v_fmac_f32_e32 v10, v21, v14
	v_fmac_f32_e32 v33, v26, v69
	v_fmac_f32_e32 v12, v27, v16
	v_fmac_f32_e32 v11, v19, v15
	v_mul_f32_e32 v9, 0x41800000, v9
	v_mul_f32_e32 v10, 0x41800000, v10
	v_mul_f32_e32 v15, 0x41800000, v33
	v_mul_f32_e32 v12, 0x41800000, v12
	v_cvt_pk_fp8_f32 v28, v9, v10
	v_cvt_pk_fp8_f32 v29, v15, v12
	v_lshlrev_b32_e32 v66, 16, v13
	v_and_b32_e32 v13, 0xffff0000, v13
	v_lshlrev_b32_e32 v70, 16, v17
	v_and_b32_e32 v17, 0xffff0000, v17
	v_fmac_f32_e32 v32, v18, v68
	v_fmac_f32_e32 v66, v24, v70
	v_fmac_f32_e32 v13, v25, v17
	v_mul_f32_e32 v14, 0x41800000, v32
	v_mul_f32_e32 v11, 0x41800000, v11
	v_mul_f32_e32 v9, 0x41800000, v66
	v_mul_f32_e32 v10, 0x41800000, v13
	v_cvt_pk_fp8_f32 v28, v14, v11 op_sel:[0,0,1]
	v_cvt_pk_fp8_f32 v29, v9, v10 op_sel:[0,0,1]
	v_lshlrev_b64 v[10:11], 12, v[30:31]
	v_lshl_add_u64 v[10:11], s[8:9], 0, v[10:11]
	v_mad_i64_i32 v[14:15], s[58:59], v30, s57, v[4:5]
	v_lshl_add_u64 v[18:19], v[10:11], 0, v[6:7]
	global_store_dwordx2 v[22:23], v[28:29], off offset:128
	v_lshl_add_u64 v[20:21], v[14:15], 0, v[6:7]
	global_load_dwordx4 v[10:13], v[18:19], off
	global_load_dwordx4 v[14:17], v[20:21], off
	v_pk_mul_f32 v[24:25], v[62:63], s[40:41] op_sel_hi:[1,0]
	v_pk_mul_f32 v[26:27], v[60:61], s[40:41] op_sel_hi:[1,0]
	v_pk_mul_f32 v[28:29], v[58:59], s[40:41] op_sel_hi:[1,0]
	v_pk_mul_f32 v[22:23], v[64:65], s[40:41] op_sel_hi:[1,0]
	v_mov_b32_e32 v32, 0
	v_mov_b32_e32 v33, 0
	s_waitcnt vmcnt(1)
	v_lshlrev_b32_e32 v9, 16, v10
	v_and_b32_e32 v10, 0xffff0000, v10
	v_lshlrev_b32_e32 v59, 16, v12
	v_and_b32_e32 v12, 0xffff0000, v12
	s_waitcnt vmcnt(0)
	v_lshlrev_b32_e32 v61, 16, v14
	v_and_b32_e32 v14, 0xffff0000, v14
	v_lshlrev_b32_e32 v63, 16, v16
	v_and_b32_e32 v16, 0xffff0000, v16
	v_lshlrev_b32_e32 v58, 16, v11
	v_and_b32_e32 v11, 0xffff0000, v11
	v_lshlrev_b32_e32 v62, 16, v15
	v_and_b32_e32 v15, 0xffff0000, v15
	v_fmac_f32_e32 v9, v24, v61
	v_fmac_f32_e32 v10, v25, v14
	v_fmac_f32_e32 v59, v28, v63
	v_fmac_f32_e32 v12, v29, v16
	v_fmac_f32_e32 v11, v23, v15
	v_mul_f32_e32 v9, 0x41800000, v9
	v_mul_f32_e32 v10, 0x41800000, v10
	v_mul_f32_e32 v15, 0x41800000, v59
	v_mul_f32_e32 v12, 0x41800000, v12
	v_cvt_pk_fp8_f32 v32, v9, v10
	v_cvt_pk_fp8_f32 v33, v15, v12
	v_lshlrev_b32_e32 v60, 16, v13
	v_and_b32_e32 v13, 0xffff0000, v13
	v_lshlrev_b32_e32 v64, 16, v17
	v_and_b32_e32 v17, 0xffff0000, v17
	v_fmac_f32_e32 v58, v22, v62
	v_fmac_f32_e32 v60, v26, v64
	v_fmac_f32_e32 v13, v27, v17
	v_mul_f32_e32 v14, 0x41800000, v58
	v_mul_f32_e32 v11, 0x41800000, v11
	v_mul_f32_e32 v9, 0x41800000, v60
	v_mul_f32_e32 v10, 0x41800000, v13
	v_cvt_pk_fp8_f32 v32, v14, v11 op_sel:[0,0,1]
	v_cvt_pk_fp8_f32 v33, v9, v10 op_sel:[0,0,1]
	v_lshlrev_b64 v[10:11], 11, v[30:31]
	v_lshl_add_u64 v[10:11], s[22:23], 0, v[10:11]
	v_lshl_add_u64 v[22:23], v[10:11], 0, v[2:3]
	global_store_dwordx2 v[22:23], v[32:33], off
	global_load_dwordx4 v[10:13], v[18:19], off offset:256
	global_load_dwordx4 v[14:17], v[20:21], off offset:256
	v_pk_mul_f32 v[20:21], v[54:55], s[40:41] op_sel_hi:[1,0]
	v_pk_mul_f32 v[24:25], v[52:53], s[40:41] op_sel_hi:[1,0]
	v_pk_mul_f32 v[26:27], v[50:51], s[40:41] op_sel_hi:[1,0]
	v_add_u32_e32 v30, 0xb0, v8
	v_mov_b32_e32 v28, 0
	v_mov_b32_e32 v29, 0
	v_pk_mul_f32 v[18:19], v[56:57], s[40:41] op_sel_hi:[1,0]
	v_ashrrev_i32_e32 v31, 31, v30
	v_mad_i64_i32 v[4:5], s[58:59], v30, s57, v[4:5]
	s_waitcnt vmcnt(1)
	v_lshlrev_b32_e32 v8, 16, v10
	v_and_b32_e32 v9, 0xffff0000, v10
	v_lshlrev_b32_e32 v32, 16, v12
	v_and_b32_e32 v12, 0xffff0000, v12
	s_waitcnt vmcnt(0)
; __device__ __forceinline__ float bf_lo(unsigned w) { return __uint_as_float(w << 16); }
; __device__ __forceinline__ float bf_hi(unsigned w) { return __uint_as_float(w & 0xffff0000u); }
;     __device__ __forceinline__ void operator()(const f32x4 (&acc)[2][2][4][2], const Unit& u, int wr, int wc, int fr, int fq) const {
;     ...
;             for (int m = 0; m < 4; ++m) { const size_t row = (size_t)(row0 + ai * HALF + m * 16);
; #pragma unroll
;                 for (int bj = 0; bj < 2; ++bj) { const int col = col0 + bj * HALF; const u32x4 g = *(const u32x4*)(G + row * ldg + col);
;                     const u32x4 mw = *(const u32x4*)(M1 + row * 2048 + col);
;                     const f32x4 m0 = {bf_lo(mw.x), bf_hi(mw.x), bf_lo(mw.y), bf_hi(mw.y)}, m1 = {bf_lo(mw.z), bf_hi(mw.z), bf_lo(mw.w), bf_hi(mw.w)};
;                     const f32x4 a0 = acc[ai][bj][m][0] * P5_ACC_SCALE, a1 = acc[ai][bj][m][1] * P5_ACC_SCALE;
;                     const f32x4 o0 = {m0[0] + a0[0] * bf_lo(g.x), m0[1] + a0[1] * bf_hi(g.x), m0[2] + a0[2] * bf_lo(g.y), m0[3] + a0[3] * bf_hi(g.y)};
;                     const f32x4 o1 = {m1[0] + a1[0] * bf_lo(g.z), m1[1] + a1[1] * bf_hi(g.z), m1[2] + a1[2] * bf_lo(g.w), m1[3] + a1[3] * bf_hi(g.w)};
;                     int w0 = __builtin_amdgcn_cvt_pk_fp8_f32(o0[0] * 16.f, o0[1] * 16.f, 0, false); w0 = __builtin_amdgcn_cvt_pk_fp8_f32(o0[2] * 16.f, o0[3] * 16.f, w0, true);
;                     int w1 = __builtin_amdgcn_cvt_pk_fp8_f32(o1[0] * 16.f, o1[1] * 16.f, 0, false); w1 = __builtin_amdgcn_cvt_pk_fp8_f32(o1[2] * 16.f, o1[3] * 16.f, w1, true);
;                     typedef int v2i_m __attribute__((ext_vector_type(2))); *(v2i_m*)(MG + row * 2048 + col) = (v2i_m){w0, w1}; } }
	v_lshlrev_b32_e32 v50, 16, v14
	v_and_b32_e32 v14, 0xffff0000, v14
	v_lshlrev_b32_e32 v52, 16, v16
	v_and_b32_e32 v16, 0xffff0000, v16
	v_fmac_f32_e32 v8, v20, v50
	v_fmac_f32_e32 v9, v21, v14
	v_fmac_f32_e32 v32, v26, v52
	v_fmac_f32_e32 v12, v27, v16
	v_mul_f32_e32 v8, 0x41800000, v8
	v_mul_f32_e32 v9, 0x41800000, v9
	v_mul_f32_e32 v14, 0x41800000, v32
	v_mul_f32_e32 v12, 0x41800000, v12
	v_cvt_pk_fp8_f32 v28, v8, v9
	v_cvt_pk_fp8_f32 v29, v14, v12
	v_lshlrev_b32_e32 v10, 16, v11
	v_and_b32_e32 v11, 0xffff0000, v11
	v_lshlrev_b32_e32 v33, 16, v13
	v_and_b32_e32 v13, 0xffff0000, v13
	v_lshlrev_b32_e32 v51, 16, v15
	v_and_b32_e32 v15, 0xffff0000, v15
	v_lshlrev_b32_e32 v53, 16, v17
	v_and_b32_e32 v17, 0xffff0000, v17
	v_fmac_f32_e32 v10, v18, v51
	v_fmac_f32_e32 v11, v19, v15
	v_fmac_f32_e32 v33, v24, v53
	v_fmac_f32_e32 v13, v25, v17
	v_mul_f32_e32 v10, 0x41800000, v10
	v_mul_f32_e32 v11, 0x41800000, v11
	v_mul_f32_e32 v8, 0x41800000, v33
	v_mul_f32_e32 v9, 0x41800000, v13
	v_cvt_pk_fp8_f32 v28, v10, v11 op_sel:[0,0,1]
	v_cvt_pk_fp8_f32 v29, v8, v9 op_sel:[0,0,1]
	v_lshlrev_b64 v[8:9], 12, v[30:31]
	v_lshl_add_u64 v[8:9], s[8:9], 0, v[8:9]
	v_lshl_add_u64 v[12:13], v[8:9], 0, v[6:7]
	global_store_dwordx2 v[22:23], v[28:29], off offset:128
	v_lshl_add_u64 v[14:15], v[4:5], 0, v[6:7]
	global_load_dwordx4 v[8:11], v[12:13], off
	global_load_dwordx4 v[4:7], v[14:15], off
	v_pk_mul_f32 v[16:17], v[48:49], s[40:41] op_sel_hi:[1,0]
	v_pk_mul_f32 v[18:19], v[46:47], s[40:41] op_sel_hi:[1,0]
	v_pk_mul_f32 v[22:23], v[42:43], s[40:41] op_sel_hi:[1,0]
	v_pk_mul_f32 v[20:21], v[44:45], s[40:41] op_sel_hi:[1,0]
	v_mov_b32_e32 v24, 0
	v_mov_b32_e32 v25, 0
	s_waitcnt vmcnt(1)
	v_lshlrev_b32_e32 v26, 16, v8
	v_and_b32_e32 v8, 0xffff0000, v8
	v_lshlrev_b32_e32 v27, 16, v9
	v_and_b32_e32 v9, 0xffff0000, v9
	v_lshlrev_b32_e32 v28, 16, v10
	v_and_b32_e32 v10, 0xffff0000, v10
	s_waitcnt vmcnt(0)
	v_lshlrev_b32_e32 v32, 16, v4
	v_and_b32_e32 v4, 0xffff0000, v4
	v_lshlrev_b32_e32 v33, 16, v5
	v_and_b32_e32 v5, 0xffff0000, v5
	v_lshlrev_b32_e32 v42, 16, v6
	v_and_b32_e32 v6, 0xffff0000, v6
	v_lshlrev_b32_e32 v29, 16, v11
	v_and_b32_e32 v11, 0xffff0000, v11
	v_lshlrev_b32_e32 v43, 16, v7
	v_and_b32_e32 v7, 0xffff0000, v7
	v_fmac_f32_e32 v26, v18, v32
	v_fmac_f32_e32 v8, v19, v4
	v_fmac_f32_e32 v9, v17, v5
	v_fmac_f32_e32 v28, v22, v42
	v_fmac_f32_e32 v10, v23, v6
	v_fmac_f32_e32 v11, v21, v7
	v_mul_f32_e32 v4, 0x41800000, v26
	v_mul_f32_e32 v5, 0x41800000, v8
	v_mul_f32_e32 v7, 0x41800000, v9
	v_mul_f32_e32 v8, 0x41800000, v28
	v_mul_f32_e32 v9, 0x41800000, v10
	v_cvt_pk_fp8_f32 v24, v4, v5
	v_cvt_pk_fp8_f32 v25, v8, v9
	v_fmac_f32_e32 v27, v16, v33
	v_fmac_f32_e32 v29, v20, v43
	v_mul_f32_e32 v6, 0x41800000, v27
	v_mul_f32_e32 v4, 0x41800000, v29
	v_mul_f32_e32 v5, 0x41800000, v11
	v_cvt_pk_fp8_f32 v24, v6, v7 op_sel:[0,0,1]
	v_cvt_pk_fp8_f32 v25, v4, v5 op_sel:[0,0,1]
	v_lshlrev_b64 v[4:5], 11, v[30:31]
	v_lshl_add_u64 v[4:5], s[22:23], 0, v[4:5]
	v_lshl_add_u64 v[10:11], v[4:5], 0, v[2:3]
	global_store_dwordx2 v[10:11], v[24:25], off
	global_load_dwordx4 v[2:5], v[12:13], off offset:256
	global_load_dwordx4 v[6:9], v[14:15], off offset:256
	v_pk_mul_f32 v[14:15], v[38:39], s[40:41] op_sel_hi:[1,0]
	v_pk_mul_f32 v[18:19], v[34:35], s[40:41] op_sel_hi:[1,0]
	v_mov_b32_e32 v20, 0
	v_mov_b32_e32 v21, 0
	v_pk_mul_f32 v[12:13], v[40:41], s[40:41] op_sel_hi:[1,0]
	v_pk_mul_f32 v[16:17], v[36:37], s[40:41] op_sel_hi:[1,0]
	s_waitcnt vmcnt(1)
	v_lshlrev_b32_e32 v22, 16, v2
	v_and_b32_e32 v2, 0xffff0000, v2
	v_lshlrev_b32_e32 v24, 16, v4
	v_and_b32_e32 v4, 0xffff0000, v4
	s_waitcnt vmcnt(0)
	v_lshlrev_b32_e32 v26, 16, v6
	v_and_b32_e32 v6, 0xffff0000, v6
	v_lshlrev_b32_e32 v28, 16, v8
	v_and_b32_e32 v8, 0xffff0000, v8
	v_fmac_f32_e32 v22, v14, v26
	v_fmac_f32_e32 v2, v15, v6
	v_fmac_f32_e32 v24, v18, v28
	v_fmac_f32_e32 v4, v19, v8
	v_mul_f32_e32 v6, 0x41800000, v22
	v_mul_f32_e32 v2, 0x41800000, v2
	v_mul_f32_e32 v8, 0x41800000, v24
	v_mul_f32_e32 v4, 0x41800000, v4
	v_cvt_pk_fp8_f32 v20, v6, v2
	v_cvt_pk_fp8_f32 v21, v8, v4
	v_lshlrev_b32_e32 v23, 16, v3
	v_and_b32_e32 v3, 0xffff0000, v3
	v_lshlrev_b32_e32 v25, 16, v5
	v_and_b32_e32 v5, 0xffff0000, v5
	v_lshlrev_b32_e32 v27, 16, v7
	v_and_b32_e32 v7, 0xffff0000, v7
	v_lshlrev_b32_e32 v29, 16, v9
	v_and_b32_e32 v9, 0xffff0000, v9
	v_fmac_f32_e32 v23, v12, v27
	v_fmac_f32_e32 v3, v13, v7
	v_fmac_f32_e32 v25, v16, v29
	v_fmac_f32_e32 v5, v17, v9
	v_mul_f32_e32 v7, 0x41800000, v23
	v_mul_f32_e32 v3, 0x41800000, v3
	v_mul_f32_e32 v2, 0x41800000, v25
	v_mul_f32_e32 v4, 0x41800000, v5
	v_cvt_pk_fp8_f32 v20, v7, v3 op_sel:[0,0,1]
	v_cvt_pk_fp8_f32 v21, v2, v4 op_sel:[0,0,1]
	global_store_dwordx2 v[10:11], v[20:21], off offset:128
	s_cbranch_vccnz .LBB0_742
	s_andn2_b64 vcc, exec, s[14:15]
	s_cbranch_vccnz .LBB0_741
	s_barrier
	s_branch .LBB0_741
